# grid barrier: waiting workgroups and XCD leaders poll the top-level arrival counter directly (target (gen+1)*nx) instead of the two-hop TOPGEN/XGEN generation flags
# baseline (speedup 1.0000x reference)
; __device__ __forceinline__ unsigned xb_ld(unsigned* p)              { return __hip_atomic_load(p, __ATOMIC_RELAXED, __HIP_MEMORY_SCOPE_AGENT); }
; __device__ __forceinline__ unsigned xb_add(unsigned* p, unsigned v) { return __hip_atomic_fetch_add(p, v, __ATOMIC_RELAXED, __HIP_MEMORY_SCOPE_AGENT); }
; #define XB_SPIN(cond, bar) do { unsigned _sp = 0; while (cond) { __builtin_amdgcn_s_sleep(1); \
;     if ((++_sp & 255u) == 0u) { if (xb_ld(&(bar)[XB_TMO])) break; if (_sp > XB_SPIN_CAP) { atomicAdd(&(bar)[XB_TMO], 1u); break; } } } } while (0)
; __device__ __forceinline__ void xcd_barrier(const XcdBarrier& b) {
;     ...
;         const unsigned old = xb_add(&bar[XB_XSUB(b.x)], 1u);
;         const unsigned gen = old / nloc;
;         if (old + 1u == (gen + 1u) * nloc) {
;             __builtin_amdgcn_fence(__ATOMIC_RELEASE, "agent");
;             asm volatile("s_waitcnt vmcnt(0)" ::: "memory");
;             const unsigned og = xb_add(&bar[XB_TOP], 1u);
;             const unsigned tg = og / nx;
;             if (og + 1u == (tg + 1u) * nx) xb_add(&bar[XB_TOPGEN], 1u);
;             else XB_SPIN(xb_ld(&bar[XB_TOPGEN]) == tg, bar);
;             xb_add(&bar[XB_XGEN(b.x)], 1u);
;             __builtin_amdgcn_fence(__ATOMIC_ACQUIRE, "agent");
;         } else {
;             XB_SPIN(xb_ld(&bar[XB_XGEN(b.x)]) == gen, bar);
.LBB0_95:
	s_or_b64 exec, exec, s[22:23]
	v_cvt_f32_u32_e32 v6, v4
	s_waitcnt vmcnt(0)
	v_readfirstlane_b32 s0, v5
	v_sub_u32_e32 v5, 0, v4
	v_rcp_iflag_f32_e32 v6, v6
	v_add_u32_e32 v7, s0, v3
	v_mul_f32_e32 v6, 0x4f7ffffe, v6
	v_cvt_u32_f32_e32 v6, v6
	v_mul_lo_u32 v3, v5, v6
	v_mul_hi_u32 v3, v6, v3
	v_add_u32_e32 v3, v6, v3
	v_mul_hi_u32 v3, v7, v3
	v_mul_lo_u32 v5, v3, v4
	v_sub_u32_e32 v5, v7, v5
	v_add_u32_e32 v6, 1, v3
	v_cmp_ge_u32_e32 vcc, v5, v4
	s_nop 1
	v_cndmask_b32_e32 v3, v3, v6, vcc
	v_sub_u32_e32 v6, v5, v4
	v_cndmask_b32_e32 v5, v5, v6, vcc
	v_add_u32_e32 v6, 1, v3
	v_cmp_ge_u32_e32 vcc, v5, v4
	v_add_u32_e32 v5, 1, v7
	s_nop 0
	v_cndmask_b32_e32 v3, v3, v6, vcc
	v_mul_lo_u32 v6, v4, v3
	v_add_u32_e32 v4, v6, v4
	v_cmp_ne_u32_e32 vcc, v5, v4
	s_and_saveexec_b64 s[0:1], vcc
	s_xor_b64 s[10:11], exec, s[0:1]
	s_cbranch_execz .LBB0_109
	s_waitcnt lgkmcnt(0)
	v_mad_u32_u24 v5, v3, v2, v2
	v_mov_b32_e32 v2, 0x4000
	global_load_dword v2, v2, s[70:71] offset:1024 sc1
	s_add_u32 s38, s70, 0x4400
	s_addc_u32 s39, s71, 0
	s_waitcnt vmcnt(0)
	v_cmp_lt_u32_e32 vcc, v2, v5
	s_and_saveexec_b64 s[22:23], vcc
	s_cbranch_execz .LBB0_108
	s_add_u32 s36, s70, 0x1200
	s_addc_u32 s37, s71, 0
	s_mov_b32 s0, 1
	s_mov_b64 s[42:43], 0
	v_mov_b32_e32 v2, 0
	s_branch .LBB0_99

; __device__ __forceinline__ unsigned xb_ld(unsigned* p)              { return __hip_atomic_load(p, __ATOMIC_RELAXED, __HIP_MEMORY_SCOPE_AGENT); }
; #define XB_SPIN(cond, bar) do { unsigned _sp = 0; while (cond) { __builtin_amdgcn_s_sleep(1); \
;     if ((++_sp & 255u) == 0u) { if (xb_ld(&(bar)[XB_TMO])) break; if (_sp > XB_SPIN_CAP) { atomicAdd(&(bar)[XB_TMO], 1u); break; } } } } while (0)
; __device__ __forceinline__ void xcd_barrier(const XcdBarrier& b) {
;     ...
;             XB_SPIN(xb_ld(&bar[XB_XGEN(b.x)]) == gen, bar);
.LBB0_101:
	global_load_dword v4, v2, s[38:39] sc1
	s_add_i32 s0, s0, 1
	s_mov_b64 s[50:51], -1
	s_waitcnt vmcnt(0)
	v_cmp_ge_u32_e32 vcc, v4, v5
	s_orn2_b64 s[46:47], vcc, exec
	s_branch .LBB0_98

; __device__ __forceinline__ unsigned xb_ld(unsigned* p)              { return __hip_atomic_load(p, __ATOMIC_RELAXED, __HIP_MEMORY_SCOPE_AGENT); }
; __device__ __forceinline__ unsigned xb_add(unsigned* p, unsigned v) { return __hip_atomic_fetch_add(p, v, __ATOMIC_RELAXED, __HIP_MEMORY_SCOPE_AGENT); }
; #define XB_SPIN(cond, bar) do { unsigned _sp = 0; while (cond) { __builtin_amdgcn_s_sleep(1); \
;     if ((++_sp & 255u) == 0u) { if (xb_ld(&(bar)[XB_TMO])) break; if (_sp > XB_SPIN_CAP) { atomicAdd(&(bar)[XB_TMO], 1u); break; } } } } while (0)
; __device__ __forceinline__ void xcd_barrier(const XcdBarrier& b) {
;     ...
;         if (old + 1u == (gen + 1u) * nloc) {
;             __builtin_amdgcn_fence(__ATOMIC_RELEASE, "agent");
;             asm volatile("s_waitcnt vmcnt(0)" ::: "memory");
;             const unsigned og = xb_add(&bar[XB_TOP], 1u);
;             const unsigned tg = og / nx;
;             if (og + 1u == (tg + 1u) * nx) xb_add(&bar[XB_TOPGEN], 1u);
;             else XB_SPIN(xb_ld(&bar[XB_TOPGEN]) == tg, bar);
.LBB0_112:
	s_or_b64 exec, exec, s[36:37]
	v_cvt_f32_u32_e32 v5, v2
	s_waitcnt vmcnt(0)
	v_readfirstlane_b32 s0, v4
	s_add_u32 s36, s70, 0x4500
	s_addc_u32 s37, s71, 0
	v_rcp_iflag_f32_e32 v5, v5
	v_add_u32_e32 v3, s0, v3
	v_add_u32_e32 v6, 1, v3
	s_mov_b64 s[38:39], -1
	v_mul_f32_e32 v4, 0x4f7ffffe, v5
	v_cvt_u32_f32_e32 v4, v4
	v_sub_u32_e32 v5, 0, v2
	v_mul_lo_u32 v5, v5, v4
	v_mul_hi_u32 v5, v4, v5
	v_add_u32_e32 v4, v4, v5
	v_mul_hi_u32 v4, v3, v4
	v_mul_lo_u32 v5, v4, v2
	v_sub_u32_e32 v3, v3, v5
	v_add_u32_e32 v7, 1, v4
	v_cmp_ge_u32_e32 vcc, v3, v2
	v_sub_u32_e32 v5, v3, v2
	s_nop 0
	v_cndmask_b32_e32 v4, v4, v7, vcc
	v_cndmask_b32_e32 v3, v3, v5, vcc
	v_add_u32_e32 v5, 1, v4
	v_cmp_ge_u32_e32 vcc, v3, v2
	s_nop 1
	v_cndmask_b32_e32 v4, v4, v5, vcc
	v_mul_lo_u32 v3, v2, v4
	v_add_u32_e32 v2, v3, v2
	v_cmp_ne_u32_e32 vcc, v6, v2
	v_mov_b32_e32 v6, v2
	v_mov_b64_e32 v[2:3], s[36:37]
	s_and_saveexec_b64 s[22:23], vcc
	s_cbranch_execz .LBB0_124
	v_mov_b32_e32 v2, 0
	global_load_dword v3, v2, s[36:37] offset:-256 sc1
	s_mov_b64 s[44:45], 0
	s_waitcnt vmcnt(0)
	v_cmp_lt_u32_e32 vcc, v3, v6
	s_and_saveexec_b64 s[42:43], vcc
	s_cbranch_execz .LBB0_123
	s_add_u32 s38, s70, 0x1200
	s_addc_u32 s39, s71, 0
	s_mov_b32 s0, 1
	s_branch .LBB0_116

; __device__ __forceinline__ unsigned xb_ld(unsigned* p)              { return __hip_atomic_load(p, __ATOMIC_RELAXED, __HIP_MEMORY_SCOPE_AGENT); }
; #define XB_SPIN(cond, bar) do { unsigned _sp = 0; while (cond) { __builtin_amdgcn_s_sleep(1); \
;     if ((++_sp & 255u) == 0u) { if (xb_ld(&(bar)[XB_TMO])) break; if (_sp > XB_SPIN_CAP) { atomicAdd(&(bar)[XB_TMO], 1u); break; } } } } while (0)
; __device__ __forceinline__ void xcd_barrier(const XcdBarrier& b) {
;     ...
;             else XB_SPIN(xb_ld(&bar[XB_TOPGEN]) == tg, bar);
.LBB0_118:
	global_load_dword v3, v2, s[36:37] offset:-256 sc1
	s_add_i32 s0, s0, 1
	s_mov_b64 s[50:51], -1
	s_waitcnt vmcnt(0)
	v_cmp_ge_u32_e32 vcc, v3, v6
	s_orn2_b64 s[54:55], vcc, exec
	s_branch .LBB0_115

; __device__ __forceinline__ unsigned xb_ld(unsigned* p)              { return __hip_atomic_load(p, __ATOMIC_RELAXED, __HIP_MEMORY_SCOPE_AGENT); }
; __device__ __forceinline__ unsigned xb_add(unsigned* p, unsigned v) { return __hip_atomic_fetch_add(p, v, __ATOMIC_RELAXED, __HIP_MEMORY_SCOPE_AGENT); }
; #define XB_SPIN(cond, bar) do { unsigned _sp = 0; while (cond) { __builtin_amdgcn_s_sleep(1); \
;     if ((++_sp & 255u) == 0u) { if (xb_ld(&(bar)[XB_TMO])) break; if (_sp > XB_SPIN_CAP) { atomicAdd(&(bar)[XB_TMO], 1u); break; } } } } while (0)
; __device__ __forceinline__ void xcd_barrier(const XcdBarrier& b) {
;     ...
;         const unsigned old = xb_add(&bar[XB_XSUB(b.x)], 1u);
;         const unsigned gen = old / nloc;
;         if (old + 1u == (gen + 1u) * nloc) {
;             __builtin_amdgcn_fence(__ATOMIC_RELEASE, "agent");
;             asm volatile("s_waitcnt vmcnt(0)" ::: "memory");
;             const unsigned og = xb_add(&bar[XB_TOP], 1u);
;             const unsigned tg = og / nx;
;             if (og + 1u == (tg + 1u) * nx) xb_add(&bar[XB_TOPGEN], 1u);
;             else XB_SPIN(xb_ld(&bar[XB_TOPGEN]) == tg, bar);
;             xb_add(&bar[XB_XGEN(b.x)], 1u);
;             __builtin_amdgcn_fence(__ATOMIC_ACQUIRE, "agent");
;         } else {
;             XB_SPIN(xb_ld(&bar[XB_XGEN(b.x)]) == gen, bar);
.LBB0_168:
	s_or_b64 exec, exec, s[38:39]
	v_cvt_f32_u32_e32 v6, v4
	s_waitcnt vmcnt(0)
	v_readfirstlane_b32 s0, v5
	v_sub_u32_e32 v5, 0, v4
	v_rcp_iflag_f32_e32 v6, v6
	v_add_u32_e32 v7, s0, v3
	v_mul_f32_e32 v6, 0x4f7ffffe, v6
	v_cvt_u32_f32_e32 v6, v6
	v_mul_lo_u32 v3, v5, v6
	v_mul_hi_u32 v3, v6, v3
	v_add_u32_e32 v3, v6, v3
	v_mul_hi_u32 v3, v7, v3
	v_mul_lo_u32 v5, v3, v4
	v_sub_u32_e32 v5, v7, v5
	v_add_u32_e32 v6, 1, v3
	v_cmp_ge_u32_e32 vcc, v5, v4
	s_nop 1
	v_cndmask_b32_e32 v3, v3, v6, vcc
	v_sub_u32_e32 v6, v5, v4
	v_cndmask_b32_e32 v5, v5, v6, vcc
	v_add_u32_e32 v6, 1, v3
	v_cmp_ge_u32_e32 vcc, v5, v4
	v_add_u32_e32 v5, 1, v7
	s_nop 0
	v_cndmask_b32_e32 v3, v3, v6, vcc
	v_mul_lo_u32 v6, v4, v3
	v_add_u32_e32 v4, v6, v4
	v_cmp_ne_u32_e32 vcc, v5, v4
	s_and_saveexec_b64 s[0:1], vcc
	s_xor_b64 s[22:23], exec, s[0:1]
	s_cbranch_execz .LBB0_182
	s_waitcnt lgkmcnt(0)
	v_mad_u32_u24 v5, v3, v2, v2
	v_mov_b32_e32 v2, 0x4000
	global_load_dword v2, v2, s[70:71] offset:1024 sc1
	s_add_u32 s44, s70, 0x4400
	s_addc_u32 s45, s71, 0
	s_waitcnt vmcnt(0)
	v_cmp_lt_u32_e32 vcc, v2, v5
	s_and_saveexec_b64 s[38:39], vcc
	s_cbranch_execz .LBB0_181
	s_add_u32 s42, s70, 0x1200
	s_addc_u32 s43, s71, 0
	s_mov_b32 s0, 1
	s_mov_b64 s[46:47], 0
	v_mov_b32_e32 v2, 0
	s_branch .LBB0_172

; __device__ __forceinline__ unsigned xb_ld(unsigned* p)              { return __hip_atomic_load(p, __ATOMIC_RELAXED, __HIP_MEMORY_SCOPE_AGENT); }
; #define XB_SPIN(cond, bar) do { unsigned _sp = 0; while (cond) { __builtin_amdgcn_s_sleep(1); \
;     if ((++_sp & 255u) == 0u) { if (xb_ld(&(bar)[XB_TMO])) break; if (_sp > XB_SPIN_CAP) { atomicAdd(&(bar)[XB_TMO], 1u); break; } } } } while (0)
; __device__ __forceinline__ void xcd_barrier(const XcdBarrier& b) {
;     ...
;             XB_SPIN(xb_ld(&bar[XB_XGEN(b.x)]) == gen, bar);
.LBB0_174:
	global_load_dword v4, v2, s[44:45] sc1
	s_add_i32 s0, s0, 1
	s_mov_b64 s[54:55], -1
	s_waitcnt vmcnt(0)
	v_cmp_ge_u32_e32 vcc, v4, v5
	s_orn2_b64 s[52:53], vcc, exec
	s_branch .LBB0_171

; __device__ __forceinline__ unsigned xb_ld(unsigned* p)              { return __hip_atomic_load(p, __ATOMIC_RELAXED, __HIP_MEMORY_SCOPE_AGENT); }
; __device__ __forceinline__ unsigned xb_add(unsigned* p, unsigned v) { return __hip_atomic_fetch_add(p, v, __ATOMIC_RELAXED, __HIP_MEMORY_SCOPE_AGENT); }
; #define XB_SPIN(cond, bar) do { unsigned _sp = 0; while (cond) { __builtin_amdgcn_s_sleep(1); \
;     if ((++_sp & 255u) == 0u) { if (xb_ld(&(bar)[XB_TMO])) break; if (_sp > XB_SPIN_CAP) { atomicAdd(&(bar)[XB_TMO], 1u); break; } } } } while (0)
; __device__ __forceinline__ void xcd_barrier(const XcdBarrier& b) {
;     ...
;         if (old + 1u == (gen + 1u) * nloc) {
;             __builtin_amdgcn_fence(__ATOMIC_RELEASE, "agent");
;             asm volatile("s_waitcnt vmcnt(0)" ::: "memory");
;             const unsigned og = xb_add(&bar[XB_TOP], 1u);
;             const unsigned tg = og / nx;
;             if (og + 1u == (tg + 1u) * nx) xb_add(&bar[XB_TOPGEN], 1u);
;             else XB_SPIN(xb_ld(&bar[XB_TOPGEN]) == tg, bar);
.LBB0_185:
	s_or_b64 exec, exec, s[42:43]
	v_cvt_f32_u32_e32 v5, v2
	s_waitcnt vmcnt(0)
	v_readfirstlane_b32 s0, v4
	s_add_u32 s42, s70, 0x4500
	s_addc_u32 s43, s71, 0
	v_rcp_iflag_f32_e32 v5, v5
	v_add_u32_e32 v3, s0, v3
	v_add_u32_e32 v6, 1, v3
	s_mov_b64 s[44:45], -1
	v_mul_f32_e32 v4, 0x4f7ffffe, v5
	v_cvt_u32_f32_e32 v4, v4
	v_sub_u32_e32 v5, 0, v2
	v_mul_lo_u32 v5, v5, v4
	v_mul_hi_u32 v5, v4, v5
	v_add_u32_e32 v4, v4, v5
	v_mul_hi_u32 v4, v3, v4
	v_mul_lo_u32 v5, v4, v2
	v_sub_u32_e32 v3, v3, v5
	v_add_u32_e32 v7, 1, v4
	v_cmp_ge_u32_e32 vcc, v3, v2
	v_sub_u32_e32 v5, v3, v2
	s_nop 0
	v_cndmask_b32_e32 v4, v4, v7, vcc
	v_cndmask_b32_e32 v3, v3, v5, vcc
	v_add_u32_e32 v5, 1, v4
	v_cmp_ge_u32_e32 vcc, v3, v2
	s_nop 1
	v_cndmask_b32_e32 v4, v4, v5, vcc
	v_mul_lo_u32 v3, v2, v4
	v_add_u32_e32 v2, v3, v2
	v_cmp_ne_u32_e32 vcc, v6, v2
	v_mov_b32_e32 v6, v2
	v_mov_b64_e32 v[2:3], s[42:43]
	s_and_saveexec_b64 s[38:39], vcc
	s_cbranch_execz .LBB0_197
	v_mov_b32_e32 v2, 0
	global_load_dword v3, v2, s[42:43] offset:-256 sc1
	s_mov_b64 s[50:51], 0
	s_waitcnt vmcnt(0)
	v_cmp_lt_u32_e32 vcc, v3, v6
	s_and_saveexec_b64 s[46:47], vcc
	s_cbranch_execz .LBB0_196
	s_add_u32 s44, s70, 0x1200
	s_addc_u32 s45, s71, 0
	s_mov_b32 s0, 1
	s_branch .LBB0_189

; __device__ __forceinline__ unsigned xb_ld(unsigned* p)              { return __hip_atomic_load(p, __ATOMIC_RELAXED, __HIP_MEMORY_SCOPE_AGENT); }
; #define XB_SPIN(cond, bar) do { unsigned _sp = 0; while (cond) { __builtin_amdgcn_s_sleep(1); \
;     if ((++_sp & 255u) == 0u) { if (xb_ld(&(bar)[XB_TMO])) break; if (_sp > XB_SPIN_CAP) { atomicAdd(&(bar)[XB_TMO], 1u); break; } } } } while (0)
; __device__ __forceinline__ void xcd_barrier(const XcdBarrier& b) {
;     ...
;             else XB_SPIN(xb_ld(&bar[XB_TOPGEN]) == tg, bar);
.LBB0_191:
	global_load_dword v3, v2, s[42:43] offset:-256 sc1
	s_add_i32 s0, s0, 1
	s_mov_b64 s[54:55], -1
	s_waitcnt vmcnt(0)
	v_cmp_ge_u32_e32 vcc, v3, v6
	s_orn2_b64 s[64:65], vcc, exec
	s_branch .LBB0_188

; __device__ __forceinline__ unsigned xb_ld(unsigned* p)              { return __hip_atomic_load(p, __ATOMIC_RELAXED, __HIP_MEMORY_SCOPE_AGENT); }
; #define XB_SPIN(cond, bar) do { unsigned _sp = 0; while (cond) { __builtin_amdgcn_s_sleep(1); \
;     if ((++_sp & 255u) == 0u) { if (xb_ld(&(bar)[XB_TMO])) break; if (_sp > XB_SPIN_CAP) { atomicAdd(&(bar)[XB_TMO], 1u); break; } } } } while (0)
; __device__ __forceinline__ void xcd_barrier(const XcdBarrier& b) {
;     ...
;             else XB_SPIN(xb_ld(&bar[XB_TOPGEN]) == tg, bar);
.LBB0_248:
	global_load_dword v3, v2, s[42:43] offset:-256 sc1
	s_add_i32 s0, s0, 1
	s_mov_b64 s[54:55], -1
	s_waitcnt vmcnt(0)
	v_cmp_ge_u32_e32 vcc, v3, v6
	s_orn2_b64 s[58:59], vcc, exec
	s_branch .LBB0_245

; __device__ __forceinline__ unsigned xb_ld(unsigned* p)              { return __hip_atomic_load(p, __ATOMIC_RELAXED, __HIP_MEMORY_SCOPE_AGENT); }
; __device__ __forceinline__ unsigned xb_add(unsigned* p, unsigned v) { return __hip_atomic_fetch_add(p, v, __ATOMIC_RELAXED, __HIP_MEMORY_SCOPE_AGENT); }
; #define XB_SPIN(cond, bar) do { unsigned _sp = 0; while (cond) { __builtin_amdgcn_s_sleep(1); \
;     if ((++_sp & 255u) == 0u) { if (xb_ld(&(bar)[XB_TMO])) break; if (_sp > XB_SPIN_CAP) { atomicAdd(&(bar)[XB_TMO], 1u); break; } } } } while (0)
; __device__ __forceinline__ void xcd_barrier(const XcdBarrier& b) {
;     ...
;         const unsigned old = xb_add(&bar[XB_XSUB(b.x)], 1u);
;         const unsigned gen = old / nloc;
;         if (old + 1u == (gen + 1u) * nloc) {
;             __builtin_amdgcn_fence(__ATOMIC_RELEASE, "agent");
;             asm volatile("s_waitcnt vmcnt(0)" ::: "memory");
;             const unsigned og = xb_add(&bar[XB_TOP], 1u);
;             const unsigned tg = og / nx;
;             if (og + 1u == (tg + 1u) * nx) xb_add(&bar[XB_TOPGEN], 1u);
;             else XB_SPIN(xb_ld(&bar[XB_TOPGEN]) == tg, bar);
;             xb_add(&bar[XB_XGEN(b.x)], 1u);
;             __builtin_amdgcn_fence(__ATOMIC_ACQUIRE, "agent");
;         } else {
;             XB_SPIN(xb_ld(&bar[XB_XGEN(b.x)]) == gen, bar);
.LBB0_298:
	s_or_b64 exec, exec, s[22:23]
	v_cvt_f32_u32_e32 v6, v4
	s_waitcnt vmcnt(0)
	v_readfirstlane_b32 s0, v5
	v_sub_u32_e32 v5, 0, v4
	v_rcp_iflag_f32_e32 v6, v6
	v_add_u32_e32 v7, s0, v3
	v_mul_f32_e32 v6, 0x4f7ffffe, v6
	v_cvt_u32_f32_e32 v6, v6
	v_mul_lo_u32 v3, v5, v6
	v_mul_hi_u32 v3, v6, v3
	v_add_u32_e32 v3, v6, v3
	v_mul_hi_u32 v3, v7, v3
	v_mul_lo_u32 v5, v3, v4
	v_sub_u32_e32 v5, v7, v5
	v_add_u32_e32 v6, 1, v3
	v_cmp_ge_u32_e32 vcc, v5, v4
	s_nop 1
	v_cndmask_b32_e32 v3, v3, v6, vcc
	v_sub_u32_e32 v6, v5, v4
	v_cndmask_b32_e32 v5, v5, v6, vcc
	v_add_u32_e32 v6, 1, v3
	v_cmp_ge_u32_e32 vcc, v5, v4
	v_add_u32_e32 v5, 1, v7
	s_nop 0
	v_cndmask_b32_e32 v3, v3, v6, vcc
	v_mul_lo_u32 v6, v4, v3
	v_add_u32_e32 v4, v6, v4
	v_cmp_ne_u32_e32 vcc, v5, v4
	s_and_saveexec_b64 s[0:1], vcc
	s_xor_b64 s[16:17], exec, s[0:1]
	s_cbranch_execz .LBB0_312
	s_waitcnt lgkmcnt(0)
	v_mad_u32_u24 v5, v3, v2, v2
	v_mov_b32_e32 v2, 0x4000
	global_load_dword v2, v2, s[70:71] offset:1024 sc1
	s_add_u32 s42, s70, 0x4400
	s_addc_u32 s43, s71, 0
	s_waitcnt vmcnt(0)
	v_cmp_lt_u32_e32 vcc, v2, v5
	s_and_saveexec_b64 s[22:23], vcc
	s_cbranch_execz .LBB0_311
	s_add_u32 s38, s70, 0x1200
	s_addc_u32 s39, s71, 0
	s_mov_b32 s0, 1
	s_mov_b64 s[44:45], 0
	v_mov_b32_e32 v2, 0
	s_branch .LBB0_302

; __device__ __forceinline__ unsigned xb_ld(unsigned* p)              { return __hip_atomic_load(p, __ATOMIC_RELAXED, __HIP_MEMORY_SCOPE_AGENT); }
; #define XB_SPIN(cond, bar) do { unsigned _sp = 0; while (cond) { __builtin_amdgcn_s_sleep(1); \
;     if ((++_sp & 255u) == 0u) { if (xb_ld(&(bar)[XB_TMO])) break; if (_sp > XB_SPIN_CAP) { atomicAdd(&(bar)[XB_TMO], 1u); break; } } } } while (0)
; __device__ __forceinline__ void xcd_barrier(const XcdBarrier& b) {
;     ...
;             XB_SPIN(xb_ld(&bar[XB_XGEN(b.x)]) == gen, bar);
.LBB0_304:
	global_load_dword v4, v2, s[42:43] sc1
	s_add_i32 s0, s0, 1
	s_mov_b64 s[52:53], -1
	s_waitcnt vmcnt(0)
	v_cmp_ge_u32_e32 vcc, v4, v5
	s_orn2_b64 s[50:51], vcc, exec
	s_branch .LBB0_301

; __device__ __forceinline__ unsigned xb_ld(unsigned* p)              { return __hip_atomic_load(p, __ATOMIC_RELAXED, __HIP_MEMORY_SCOPE_AGENT); }
; __device__ __forceinline__ unsigned xb_add(unsigned* p, unsigned v) { return __hip_atomic_fetch_add(p, v, __ATOMIC_RELAXED, __HIP_MEMORY_SCOPE_AGENT); }
; #define XB_SPIN(cond, bar) do { unsigned _sp = 0; while (cond) { __builtin_amdgcn_s_sleep(1); \
;     if ((++_sp & 255u) == 0u) { if (xb_ld(&(bar)[XB_TMO])) break; if (_sp > XB_SPIN_CAP) { atomicAdd(&(bar)[XB_TMO], 1u); break; } } } } while (0)
; __device__ __forceinline__ void xcd_barrier(const XcdBarrier& b) {
;     ...
;         if (old + 1u == (gen + 1u) * nloc) {
;             __builtin_amdgcn_fence(__ATOMIC_RELEASE, "agent");
;             asm volatile("s_waitcnt vmcnt(0)" ::: "memory");
;             const unsigned og = xb_add(&bar[XB_TOP], 1u);
;             const unsigned tg = og / nx;
;             if (og + 1u == (tg + 1u) * nx) xb_add(&bar[XB_TOPGEN], 1u);
;             else XB_SPIN(xb_ld(&bar[XB_TOPGEN]) == tg, bar);
.LBB0_315:
	s_or_b64 exec, exec, s[38:39]
	v_cvt_f32_u32_e32 v5, v2
	s_waitcnt vmcnt(0)
	v_readfirstlane_b32 s0, v4
	s_add_u32 s38, s70, 0x4500
	s_addc_u32 s39, s71, 0
	v_rcp_iflag_f32_e32 v5, v5
	v_add_u32_e32 v3, s0, v3
	v_add_u32_e32 v6, 1, v3
	s_mov_b64 s[42:43], -1
	v_mul_f32_e32 v4, 0x4f7ffffe, v5
	v_cvt_u32_f32_e32 v4, v4
	v_sub_u32_e32 v5, 0, v2
	v_mul_lo_u32 v5, v5, v4
	v_mul_hi_u32 v5, v4, v5
	v_add_u32_e32 v4, v4, v5
	v_mul_hi_u32 v4, v3, v4
	v_mul_lo_u32 v5, v4, v2
	v_sub_u32_e32 v3, v3, v5
	v_add_u32_e32 v7, 1, v4
	v_cmp_ge_u32_e32 vcc, v3, v2
	v_sub_u32_e32 v5, v3, v2
	s_nop 0
	v_cndmask_b32_e32 v4, v4, v7, vcc
	v_cndmask_b32_e32 v3, v3, v5, vcc
	v_add_u32_e32 v5, 1, v4
	v_cmp_ge_u32_e32 vcc, v3, v2
	s_nop 1
	v_cndmask_b32_e32 v4, v4, v5, vcc
	v_mul_lo_u32 v3, v2, v4
	v_add_u32_e32 v2, v3, v2
	v_cmp_ne_u32_e32 vcc, v6, v2
	v_mov_b32_e32 v6, v2
	v_mov_b64_e32 v[2:3], s[38:39]
	s_and_saveexec_b64 s[22:23], vcc
	s_cbranch_execz .LBB0_327
	v_mov_b32_e32 v2, 0
	global_load_dword v3, v2, s[38:39] offset:-256 sc1
	s_mov_b64 s[46:47], 0
	s_waitcnt vmcnt(0)
	v_cmp_lt_u32_e32 vcc, v3, v6
	s_and_saveexec_b64 s[44:45], vcc
	s_cbranch_execz .LBB0_326
	s_add_u32 s42, s70, 0x1200
	s_addc_u32 s43, s71, 0
	s_mov_b32 s0, 1
	s_branch .LBB0_319

; __device__ __forceinline__ unsigned xb_ld(unsigned* p)              { return __hip_atomic_load(p, __ATOMIC_RELAXED, __HIP_MEMORY_SCOPE_AGENT); }
; #define XB_SPIN(cond, bar) do { unsigned _sp = 0; while (cond) { __builtin_amdgcn_s_sleep(1); \
;     if ((++_sp & 255u) == 0u) { if (xb_ld(&(bar)[XB_TMO])) break; if (_sp > XB_SPIN_CAP) { atomicAdd(&(bar)[XB_TMO], 1u); break; } } } } while (0)
; __device__ __forceinline__ void xcd_barrier(const XcdBarrier& b) {
;     ...
;             else XB_SPIN(xb_ld(&bar[XB_TOPGEN]) == tg, bar);
.LBB0_321:
	global_load_dword v3, v2, s[38:39] offset:-256 sc1
	s_add_i32 s0, s0, 1
	s_mov_b64 s[52:53], -1
	s_waitcnt vmcnt(0)
	v_cmp_ge_u32_e32 vcc, v3, v6
	s_orn2_b64 s[56:57], vcc, exec
	s_branch .LBB0_318

; __device__ __forceinline__ unsigned xb_ld(unsigned* p)              { return __hip_atomic_load(p, __ATOMIC_RELAXED, __HIP_MEMORY_SCOPE_AGENT); }
; __device__ __forceinline__ unsigned xb_add(unsigned* p, unsigned v) { return __hip_atomic_fetch_add(p, v, __ATOMIC_RELAXED, __HIP_MEMORY_SCOPE_AGENT); }
; #define XB_SPIN(cond, bar) do { unsigned _sp = 0; while (cond) { __builtin_amdgcn_s_sleep(1); \
;     if ((++_sp & 255u) == 0u) { if (xb_ld(&(bar)[XB_TMO])) break; if (_sp > XB_SPIN_CAP) { atomicAdd(&(bar)[XB_TMO], 1u); break; } } } } while (0)
; __device__ __forceinline__ void xcd_barrier(const XcdBarrier& b) {
;     ...
;         const unsigned old = xb_add(&bar[XB_XSUB(b.x)], 1u);
;         const unsigned gen = old / nloc;
;         if (old + 1u == (gen + 1u) * nloc) {
;             __builtin_amdgcn_fence(__ATOMIC_RELEASE, "agent");
;             asm volatile("s_waitcnt vmcnt(0)" ::: "memory");
;             const unsigned og = xb_add(&bar[XB_TOP], 1u);
;             const unsigned tg = og / nx;
;             if (og + 1u == (tg + 1u) * nx) xb_add(&bar[XB_TOPGEN], 1u);
;             else XB_SPIN(xb_ld(&bar[XB_TOPGEN]) == tg, bar);
;             xb_add(&bar[XB_XGEN(b.x)], 1u);
;             __builtin_amdgcn_fence(__ATOMIC_ACQUIRE, "agent");
;         } else {
;             XB_SPIN(xb_ld(&bar[XB_XGEN(b.x)]) == gen, bar);
.LBB0_356:
	s_or_b64 exec, exec, s[38:39]
	v_cvt_f32_u32_e32 v6, v4
	s_waitcnt vmcnt(0)
	v_readfirstlane_b32 s0, v5
	v_sub_u32_e32 v5, 0, v4
	v_rcp_iflag_f32_e32 v6, v6
	v_add_u32_e32 v7, s0, v3
	v_mul_f32_e32 v6, 0x4f7ffffe, v6
	v_cvt_u32_f32_e32 v6, v6
	v_mul_lo_u32 v3, v5, v6
	v_mul_hi_u32 v3, v6, v3
	v_add_u32_e32 v3, v6, v3
	v_mul_hi_u32 v3, v7, v3
	v_mul_lo_u32 v5, v3, v4
	v_sub_u32_e32 v5, v7, v5
	v_add_u32_e32 v6, 1, v3
	v_cmp_ge_u32_e32 vcc, v5, v4
	s_nop 1
	v_cndmask_b32_e32 v3, v3, v6, vcc
	v_sub_u32_e32 v6, v5, v4
	v_cndmask_b32_e32 v5, v5, v6, vcc
	v_add_u32_e32 v6, 1, v3
	v_cmp_ge_u32_e32 vcc, v5, v4
	v_add_u32_e32 v5, 1, v7
	s_nop 0
	v_cndmask_b32_e32 v3, v3, v6, vcc
	v_mul_lo_u32 v6, v4, v3
	v_add_u32_e32 v4, v6, v4
	v_cmp_ne_u32_e32 vcc, v5, v4
	s_and_saveexec_b64 s[0:1], vcc
	s_xor_b64 s[16:17], exec, s[0:1]
	s_cbranch_execz .LBB0_370
	s_waitcnt lgkmcnt(0)
	v_mad_u32_u24 v5, v3, v2, v2
	v_mov_b32_e32 v2, 0x4000
	global_load_dword v2, v2, s[70:71] offset:1024 sc1
	s_add_u32 s44, s70, 0x4400
	s_addc_u32 s45, s71, 0
	s_waitcnt vmcnt(0)
	v_cmp_lt_u32_e32 vcc, v2, v5
	s_and_saveexec_b64 s[38:39], vcc
	s_cbranch_execz .LBB0_369
	s_add_u32 s42, s70, 0x1200
	s_addc_u32 s43, s71, 0
	s_mov_b32 s0, 1
	s_mov_b64 s[46:47], 0
	v_mov_b32_e32 v2, 0
	s_branch .LBB0_360

; __device__ __forceinline__ unsigned xb_ld(unsigned* p)              { return __hip_atomic_load(p, __ATOMIC_RELAXED, __HIP_MEMORY_SCOPE_AGENT); }
; __device__ __forceinline__ unsigned xb_add(unsigned* p, unsigned v) { return __hip_atomic_fetch_add(p, v, __ATOMIC_RELAXED, __HIP_MEMORY_SCOPE_AGENT); }
; #define XB_SPIN(cond, bar) do { unsigned _sp = 0; while (cond) { __builtin_amdgcn_s_sleep(1); \
;     if ((++_sp & 255u) == 0u) { if (xb_ld(&(bar)[XB_TMO])) break; if (_sp > XB_SPIN_CAP) { atomicAdd(&(bar)[XB_TMO], 1u); break; } } } } while (0)
; __device__ __forceinline__ void xcd_barrier(const XcdBarrier& b) {
;     ...
;         if (old + 1u == (gen + 1u) * nloc) {
;             __builtin_amdgcn_fence(__ATOMIC_RELEASE, "agent");
;             asm volatile("s_waitcnt vmcnt(0)" ::: "memory");
;             const unsigned og = xb_add(&bar[XB_TOP], 1u);
;             const unsigned tg = og / nx;
;             if (og + 1u == (tg + 1u) * nx) xb_add(&bar[XB_TOPGEN], 1u);
;             else XB_SPIN(xb_ld(&bar[XB_TOPGEN]) == tg, bar);
.LBB0_373:
	s_or_b64 exec, exec, s[38:39]
	v_cvt_f32_u32_e32 v5, v2
	s_waitcnt vmcnt(0)
	v_readfirstlane_b32 s0, v4
	s_add_u32 s38, s70, 0x4500
	s_addc_u32 s39, s71, 0
	v_rcp_iflag_f32_e32 v5, v5
	v_add_u32_e32 v3, s0, v3
	v_add_u32_e32 v6, 1, v3
	s_mov_b64 s[42:43], -1
	v_mul_f32_e32 v4, 0x4f7ffffe, v5
	v_cvt_u32_f32_e32 v4, v4
	v_sub_u32_e32 v5, 0, v2
	v_mul_lo_u32 v5, v5, v4
	v_mul_hi_u32 v5, v4, v5
	v_add_u32_e32 v4, v4, v5
	v_mul_hi_u32 v4, v3, v4
	v_mul_lo_u32 v5, v4, v2
	v_sub_u32_e32 v3, v3, v5
	v_add_u32_e32 v7, 1, v4
	v_cmp_ge_u32_e32 vcc, v3, v2
	v_sub_u32_e32 v5, v3, v2
	s_nop 0
	v_cndmask_b32_e32 v4, v4, v7, vcc
	v_cndmask_b32_e32 v3, v3, v5, vcc
	v_add_u32_e32 v5, 1, v4
	v_cmp_ge_u32_e32 vcc, v3, v2
	s_nop 1
	v_cndmask_b32_e32 v4, v4, v5, vcc
	v_mul_lo_u32 v3, v2, v4
	v_add_u32_e32 v2, v3, v2
	v_cmp_ne_u32_e32 vcc, v6, v2
	v_mov_b32_e32 v6, v2
	v_mov_b64_e32 v[2:3], s[38:39]
	s_and_saveexec_b64 s[16:17], vcc
	s_cbranch_execz .LBB0_385
	v_mov_b32_e32 v2, 0
	global_load_dword v3, v2, s[38:39] offset:-256 sc1
	s_mov_b64 s[46:47], 0
	s_waitcnt vmcnt(0)
	v_cmp_lt_u32_e32 vcc, v3, v6
	s_and_saveexec_b64 s[44:45], vcc
	s_cbranch_execz .LBB0_384
	s_add_u32 s42, s70, 0x1200
	s_addc_u32 s43, s71, 0
	s_mov_b32 s0, 1
	s_branch .LBB0_377

; __device__ __forceinline__ unsigned xb_ld(unsigned* p)              { return __hip_atomic_load(p, __ATOMIC_RELAXED, __HIP_MEMORY_SCOPE_AGENT); }
; __device__ __forceinline__ unsigned xb_add(unsigned* p, unsigned v) { return __hip_atomic_fetch_add(p, v, __ATOMIC_RELAXED, __HIP_MEMORY_SCOPE_AGENT); }
; #define XB_SPIN(cond, bar) do { unsigned _sp = 0; while (cond) { __builtin_amdgcn_s_sleep(1); \
;     if ((++_sp & 255u) == 0u) { if (xb_ld(&(bar)[XB_TMO])) break; if (_sp > XB_SPIN_CAP) { atomicAdd(&(bar)[XB_TMO], 1u); break; } } } } while (0)
; __device__ __forceinline__ void xcd_barrier(const XcdBarrier& b) {
;     ...
;         const unsigned old = xb_add(&bar[XB_XSUB(b.x)], 1u);
;         const unsigned gen = old / nloc;
;         if (old + 1u == (gen + 1u) * nloc) {
;             __builtin_amdgcn_fence(__ATOMIC_RELEASE, "agent");
;             asm volatile("s_waitcnt vmcnt(0)" ::: "memory");
;             const unsigned og = xb_add(&bar[XB_TOP], 1u);
;             const unsigned tg = og / nx;
;             if (og + 1u == (tg + 1u) * nx) xb_add(&bar[XB_TOPGEN], 1u);
;             else XB_SPIN(xb_ld(&bar[XB_TOPGEN]) == tg, bar);
;             xb_add(&bar[XB_XGEN(b.x)], 1u);
;             __builtin_amdgcn_fence(__ATOMIC_ACQUIRE, "agent");
;         } else {
;             XB_SPIN(xb_ld(&bar[XB_XGEN(b.x)]) == gen, bar);
.LBB0_494:
	s_or_b64 exec, exec, s[42:43]
	v_cvt_f32_u32_e32 v6, v4
	s_waitcnt vmcnt(0)
	v_readfirstlane_b32 s0, v5
	v_sub_u32_e32 v5, 0, v4
	v_rcp_iflag_f32_e32 v6, v6
	v_add_u32_e32 v7, s0, v3
	v_mul_f32_e32 v6, 0x4f7ffffe, v6
	v_cvt_u32_f32_e32 v6, v6
	v_mul_lo_u32 v3, v5, v6
	v_mul_hi_u32 v3, v6, v3
	v_add_u32_e32 v3, v6, v3
	v_mul_hi_u32 v3, v7, v3
	v_mul_lo_u32 v5, v3, v4
	v_sub_u32_e32 v5, v7, v5
	v_add_u32_e32 v6, 1, v3
	v_cmp_ge_u32_e32 vcc, v5, v4
	s_nop 1
	v_cndmask_b32_e32 v3, v3, v6, vcc
	v_sub_u32_e32 v6, v5, v4
	v_cndmask_b32_e32 v5, v5, v6, vcc
	v_add_u32_e32 v6, 1, v3
	v_cmp_ge_u32_e32 vcc, v5, v4
	v_add_u32_e32 v5, 1, v7
	s_nop 0
	v_cndmask_b32_e32 v3, v3, v6, vcc
	v_mul_lo_u32 v6, v4, v3
	v_add_u32_e32 v4, v6, v4
	v_cmp_ne_u32_e32 vcc, v5, v4
	s_and_saveexec_b64 s[0:1], vcc
	s_xor_b64 s[38:39], exec, s[0:1]
	s_cbranch_execz .LBB0_508
	s_waitcnt lgkmcnt(0)
	v_mad_u32_u24 v5, v3, v2, v2
	v_mov_b32_e32 v2, 0x4000
	global_load_dword v2, v2, s[70:71] offset:1024 sc1
	s_add_u32 s46, s70, 0x4400
	s_addc_u32 s47, s71, 0
	s_waitcnt vmcnt(0)
	v_cmp_lt_u32_e32 vcc, v2, v5
	s_and_saveexec_b64 s[42:43], vcc
	s_cbranch_execz .LBB0_507
	s_add_u32 s44, s70, 0x1200
	s_addc_u32 s45, s71, 0
	s_mov_b32 s0, 1
	s_mov_b64 s[50:51], 0
	v_mov_b32_e32 v2, 0
	s_branch .LBB0_498

; __device__ __forceinline__ unsigned xb_ld(unsigned* p)              { return __hip_atomic_load(p, __ATOMIC_RELAXED, __HIP_MEMORY_SCOPE_AGENT); }
; #define XB_SPIN(cond, bar) do { unsigned _sp = 0; while (cond) { __builtin_amdgcn_s_sleep(1); \
;     if ((++_sp & 255u) == 0u) { if (xb_ld(&(bar)[XB_TMO])) break; if (_sp > XB_SPIN_CAP) { atomicAdd(&(bar)[XB_TMO], 1u); break; } } } } while (0)
; __device__ __forceinline__ void xcd_barrier(const XcdBarrier& b) {
;     ...
;             XB_SPIN(xb_ld(&bar[XB_XGEN(b.x)]) == gen, bar);
.LBB0_500:
	global_load_dword v4, v2, s[46:47] sc1
	s_add_i32 s0, s0, 1
	s_mov_b64 s[56:57], -1
	s_waitcnt vmcnt(0)
	v_cmp_ge_u32_e32 vcc, v4, v5
	s_orn2_b64 s[54:55], vcc, exec
	s_branch .LBB0_497

; __device__ __forceinline__ unsigned xb_ld(unsigned* p)              { return __hip_atomic_load(p, __ATOMIC_RELAXED, __HIP_MEMORY_SCOPE_AGENT); }
; __device__ __forceinline__ unsigned xb_add(unsigned* p, unsigned v) { return __hip_atomic_fetch_add(p, v, __ATOMIC_RELAXED, __HIP_MEMORY_SCOPE_AGENT); }
; #define XB_SPIN(cond, bar) do { unsigned _sp = 0; while (cond) { __builtin_amdgcn_s_sleep(1); \
;     if ((++_sp & 255u) == 0u) { if (xb_ld(&(bar)[XB_TMO])) break; if (_sp > XB_SPIN_CAP) { atomicAdd(&(bar)[XB_TMO], 1u); break; } } } } while (0)
; __device__ __forceinline__ void xcd_barrier(const XcdBarrier& b) {
;     ...
;         if (old + 1u == (gen + 1u) * nloc) {
;             __builtin_amdgcn_fence(__ATOMIC_RELEASE, "agent");
;             asm volatile("s_waitcnt vmcnt(0)" ::: "memory");
;             const unsigned og = xb_add(&bar[XB_TOP], 1u);
;             const unsigned tg = og / nx;
;             if (og + 1u == (tg + 1u) * nx) xb_add(&bar[XB_TOPGEN], 1u);
;             else XB_SPIN(xb_ld(&bar[XB_TOPGEN]) == tg, bar);
.LBB0_511:
	s_or_b64 exec, exec, s[44:45]
	v_cvt_f32_u32_e32 v5, v2
	s_waitcnt vmcnt(0)
	v_readfirstlane_b32 s0, v4
	s_add_u32 s44, s70, 0x4500
	s_addc_u32 s45, s71, 0
	v_rcp_iflag_f32_e32 v5, v5
	v_add_u32_e32 v3, s0, v3
	v_add_u32_e32 v6, 1, v3
	s_mov_b64 s[46:47], -1
	v_mul_f32_e32 v4, 0x4f7ffffe, v5
	v_cvt_u32_f32_e32 v4, v4
	v_sub_u32_e32 v5, 0, v2
	v_mul_lo_u32 v5, v5, v4
	v_mul_hi_u32 v5, v4, v5
	v_add_u32_e32 v4, v4, v5
	v_mul_hi_u32 v4, v3, v4
	v_mul_lo_u32 v5, v4, v2
	v_sub_u32_e32 v3, v3, v5
	v_add_u32_e32 v7, 1, v4
	v_cmp_ge_u32_e32 vcc, v3, v2
	v_sub_u32_e32 v5, v3, v2
	s_nop 0
	v_cndmask_b32_e32 v4, v4, v7, vcc
	v_cndmask_b32_e32 v3, v3, v5, vcc
	v_add_u32_e32 v5, 1, v4
	v_cmp_ge_u32_e32 vcc, v3, v2
	s_nop 1
	v_cndmask_b32_e32 v4, v4, v5, vcc
	v_mul_lo_u32 v3, v2, v4
	v_add_u32_e32 v2, v3, v2
	v_cmp_ne_u32_e32 vcc, v6, v2
	v_mov_b32_e32 v6, v2
	v_mov_b64_e32 v[2:3], s[44:45]
	s_and_saveexec_b64 s[42:43], vcc
	s_cbranch_execz .LBB0_523
	v_mov_b32_e32 v2, 0
	global_load_dword v3, v2, s[44:45] offset:-256 sc1
	s_mov_b64 s[52:53], 0
	s_waitcnt vmcnt(0)
	v_cmp_lt_u32_e32 vcc, v3, v6
	s_and_saveexec_b64 s[50:51], vcc
	s_cbranch_execz .LBB0_522
	s_add_u32 s46, s70, 0x1200
	s_addc_u32 s47, s71, 0
	s_mov_b32 s0, 1
	s_branch .LBB0_515

; __device__ __forceinline__ unsigned xb_ld(unsigned* p)              { return __hip_atomic_load(p, __ATOMIC_RELAXED, __HIP_MEMORY_SCOPE_AGENT); }
; #define XB_SPIN(cond, bar) do { unsigned _sp = 0; while (cond) { __builtin_amdgcn_s_sleep(1); \
;     if ((++_sp & 255u) == 0u) { if (xb_ld(&(bar)[XB_TMO])) break; if (_sp > XB_SPIN_CAP) { atomicAdd(&(bar)[XB_TMO], 1u); break; } } } } while (0)
; __device__ __forceinline__ void xcd_barrier(const XcdBarrier& b) {
;     ...
;             else XB_SPIN(xb_ld(&bar[XB_TOPGEN]) == tg, bar);
.LBB0_517:
	global_load_dword v3, v2, s[44:45] offset:-256 sc1
	s_add_i32 s0, s0, 1
	s_mov_b64 s[56:57], -1
	s_waitcnt vmcnt(0)
	v_cmp_ge_u32_e32 vcc, v3, v6
	s_orn2_b64 s[60:61], vcc, exec
	s_branch .LBB0_514

; __device__ __forceinline__ unsigned xb_ld(unsigned* p)              { return __hip_atomic_load(p, __ATOMIC_RELAXED, __HIP_MEMORY_SCOPE_AGENT); }
; __device__ __forceinline__ unsigned xb_add(unsigned* p, unsigned v) { return __hip_atomic_fetch_add(p, v, __ATOMIC_RELAXED, __HIP_MEMORY_SCOPE_AGENT); }
; #define XB_SPIN(cond, bar) do { unsigned _sp = 0; while (cond) { __builtin_amdgcn_s_sleep(1); \
;     if ((++_sp & 255u) == 0u) { if (xb_ld(&(bar)[XB_TMO])) break; if (_sp > XB_SPIN_CAP) { atomicAdd(&(bar)[XB_TMO], 1u); break; } } } } while (0)
; __device__ __forceinline__ void xcd_barrier(const XcdBarrier& b) {
;     ...
;         const unsigned old = xb_add(&bar[XB_XSUB(b.x)], 1u);
;         const unsigned gen = old / nloc;
;         if (old + 1u == (gen + 1u) * nloc) {
;             __builtin_amdgcn_fence(__ATOMIC_RELEASE, "agent");
;             asm volatile("s_waitcnt vmcnt(0)" ::: "memory");
;             const unsigned og = xb_add(&bar[XB_TOP], 1u);
;             const unsigned tg = og / nx;
;             if (og + 1u == (tg + 1u) * nx) xb_add(&bar[XB_TOPGEN], 1u);
;             else XB_SPIN(xb_ld(&bar[XB_TOPGEN]) == tg, bar);
;             xb_add(&bar[XB_XGEN(b.x)], 1u);
;             __builtin_amdgcn_fence(__ATOMIC_ACQUIRE, "agent");
;         } else {
;             XB_SPIN(xb_ld(&bar[XB_XGEN(b.x)]) == gen, bar);
.LBB0_550:
	s_or_b64 exec, exec, s[40:41]
	v_cvt_f32_u32_e32 v6, v4
	s_waitcnt vmcnt(0)
	v_readfirstlane_b32 s0, v5
	v_sub_u32_e32 v5, 0, v4
	v_rcp_iflag_f32_e32 v6, v6
	v_add_u32_e32 v7, s0, v3
	v_mul_f32_e32 v6, 0x4f7ffffe, v6
	v_cvt_u32_f32_e32 v6, v6
	v_mul_lo_u32 v3, v5, v6
	v_mul_hi_u32 v3, v6, v3
	v_add_u32_e32 v3, v6, v3
	v_mul_hi_u32 v3, v7, v3
	v_mul_lo_u32 v5, v3, v4
	v_sub_u32_e32 v5, v7, v5
	v_add_u32_e32 v6, 1, v3
	v_cmp_ge_u32_e32 vcc, v5, v4
	s_nop 1
	v_cndmask_b32_e32 v3, v3, v6, vcc
	v_sub_u32_e32 v6, v5, v4
	v_cndmask_b32_e32 v5, v5, v6, vcc
	v_add_u32_e32 v6, 1, v3
	v_cmp_ge_u32_e32 vcc, v5, v4
	v_add_u32_e32 v5, 1, v7
	s_nop 0
	v_cndmask_b32_e32 v3, v3, v6, vcc
	v_mul_lo_u32 v6, v4, v3
	v_add_u32_e32 v4, v6, v4
	v_cmp_ne_u32_e32 vcc, v5, v4
	s_and_saveexec_b64 s[0:1], vcc
	s_xor_b64 s[38:39], exec, s[0:1]
	s_cbranch_execz .LBB0_564
	s_waitcnt lgkmcnt(0)
	v_mad_u32_u24 v5, v3, v2, v2
	v_mov_b32_e32 v2, 0x4000
	global_load_dword v2, v2, s[70:71] offset:1024 sc1
	s_add_u32 s44, s70, 0x4400
	s_addc_u32 s45, s71, 0
	s_waitcnt vmcnt(0)
	v_cmp_lt_u32_e32 vcc, v2, v5
	s_and_saveexec_b64 s[40:41], vcc
	s_cbranch_execz .LBB0_563
	s_add_u32 s42, s70, 0x1200
	s_addc_u32 s43, s71, 0
	s_mov_b32 s0, 1
	s_mov_b64 s[46:47], 0
	v_mov_b32_e32 v2, 0
	s_branch .LBB0_554

; __device__ __forceinline__ unsigned xb_ld(unsigned* p)              { return __hip_atomic_load(p, __ATOMIC_RELAXED, __HIP_MEMORY_SCOPE_AGENT); }
; __device__ __forceinline__ unsigned xb_add(unsigned* p, unsigned v) { return __hip_atomic_fetch_add(p, v, __ATOMIC_RELAXED, __HIP_MEMORY_SCOPE_AGENT); }
; #define XB_SPIN(cond, bar) do { unsigned _sp = 0; while (cond) { __builtin_amdgcn_s_sleep(1); \
;     if ((++_sp & 255u) == 0u) { if (xb_ld(&(bar)[XB_TMO])) break; if (_sp > XB_SPIN_CAP) { atomicAdd(&(bar)[XB_TMO], 1u); break; } } } } while (0)
; __device__ __forceinline__ void xcd_barrier(const XcdBarrier& b) {
;     ...
;         if (old + 1u == (gen + 1u) * nloc) {
;             __builtin_amdgcn_fence(__ATOMIC_RELEASE, "agent");
;             asm volatile("s_waitcnt vmcnt(0)" ::: "memory");
;             const unsigned og = xb_add(&bar[XB_TOP], 1u);
;             const unsigned tg = og / nx;
;             if (og + 1u == (tg + 1u) * nx) xb_add(&bar[XB_TOPGEN], 1u);
;             else XB_SPIN(xb_ld(&bar[XB_TOPGEN]) == tg, bar);
.LBB0_567:
	s_or_b64 exec, exec, s[42:43]
	v_cvt_f32_u32_e32 v5, v2
	s_waitcnt vmcnt(0)
	v_readfirstlane_b32 s0, v4
	s_add_u32 s42, s70, 0x4500
	s_addc_u32 s43, s71, 0
	v_rcp_iflag_f32_e32 v5, v5
	v_add_u32_e32 v3, s0, v3
	v_add_u32_e32 v6, 1, v3
	s_mov_b64 s[44:45], -1
	v_mul_f32_e32 v4, 0x4f7ffffe, v5
	v_cvt_u32_f32_e32 v4, v4
	v_sub_u32_e32 v5, 0, v2
	v_mul_lo_u32 v5, v5, v4
	v_mul_hi_u32 v5, v4, v5
	v_add_u32_e32 v4, v4, v5
	v_mul_hi_u32 v4, v3, v4
	v_mul_lo_u32 v5, v4, v2
	v_sub_u32_e32 v3, v3, v5
	v_add_u32_e32 v7, 1, v4
	v_cmp_ge_u32_e32 vcc, v3, v2
	v_sub_u32_e32 v5, v3, v2
	s_nop 0
	v_cndmask_b32_e32 v4, v4, v7, vcc
	v_cndmask_b32_e32 v3, v3, v5, vcc
	v_add_u32_e32 v5, 1, v4
	v_cmp_ge_u32_e32 vcc, v3, v2
	s_nop 1
	v_cndmask_b32_e32 v4, v4, v5, vcc
	v_mul_lo_u32 v3, v2, v4
	v_add_u32_e32 v2, v3, v2
	v_cmp_ne_u32_e32 vcc, v6, v2
	v_mov_b32_e32 v6, v2
	v_mov_b64_e32 v[2:3], s[42:43]
	s_and_saveexec_b64 s[40:41], vcc
	s_cbranch_execz .LBB0_579
	v_mov_b32_e32 v2, 0
	global_load_dword v3, v2, s[42:43] offset:-256 sc1
	s_mov_b64 s[50:51], 0
	s_waitcnt vmcnt(0)
	v_cmp_lt_u32_e32 vcc, v3, v6
	s_and_saveexec_b64 s[46:47], vcc
	s_cbranch_execz .LBB0_578
	s_add_u32 s44, s70, 0x1200
	s_addc_u32 s45, s71, 0
	s_mov_b32 s0, 1
	s_branch .LBB0_571

; __device__ __forceinline__ unsigned xb_ld(unsigned* p)              { return __hip_atomic_load(p, __ATOMIC_RELAXED, __HIP_MEMORY_SCOPE_AGENT); }
; #define XB_SPIN(cond, bar) do { unsigned _sp = 0; while (cond) { __builtin_amdgcn_s_sleep(1); \
;     if ((++_sp & 255u) == 0u) { if (xb_ld(&(bar)[XB_TMO])) break; if (_sp > XB_SPIN_CAP) { atomicAdd(&(bar)[XB_TMO], 1u); break; } } } } while (0)
; __device__ __forceinline__ void xcd_barrier(const XcdBarrier& b) {
;     ...
;             XB_SPIN(xb_ld(&bar[XB_XGEN(b.x)]) == gen, bar);
.LBB0_754:
	global_load_dword v4, v2, s[44:45] sc1
	s_add_i32 s0, s0, 1
	s_mov_b64 s[52:53], -1
	s_waitcnt vmcnt(0)
	v_cmp_ge_u32_e32 vcc, v4, v5
	s_orn2_b64 s[50:51], vcc, exec
	s_branch .LBB0_751

; __device__ __forceinline__ unsigned xb_ld(unsigned* p)              { return __hip_atomic_load(p, __ATOMIC_RELAXED, __HIP_MEMORY_SCOPE_AGENT); }
; __device__ __forceinline__ unsigned xb_add(unsigned* p, unsigned v) { return __hip_atomic_fetch_add(p, v, __ATOMIC_RELAXED, __HIP_MEMORY_SCOPE_AGENT); }
; #define XB_SPIN(cond, bar) do { unsigned _sp = 0; while (cond) { __builtin_amdgcn_s_sleep(1); \
;     if ((++_sp & 255u) == 0u) { if (xb_ld(&(bar)[XB_TMO])) break; if (_sp > XB_SPIN_CAP) { atomicAdd(&(bar)[XB_TMO], 1u); break; } } } } while (0)
; __device__ __forceinline__ void xcd_barrier(const XcdBarrier& b) {
;     ...
;         if (old + 1u == (gen + 1u) * nloc) {
;             __builtin_amdgcn_fence(__ATOMIC_RELEASE, "agent");
;             asm volatile("s_waitcnt vmcnt(0)" ::: "memory");
;             const unsigned og = xb_add(&bar[XB_TOP], 1u);
;             const unsigned tg = og / nx;
;             if (og + 1u == (tg + 1u) * nx) xb_add(&bar[XB_TOPGEN], 1u);
;             else XB_SPIN(xb_ld(&bar[XB_TOPGEN]) == tg, bar);
.LBB0_765:
	s_or_b64 exec, exec, s[42:43]
	v_cvt_f32_u32_e32 v5, v2
	s_waitcnt vmcnt(0)
	v_readfirstlane_b32 s0, v4
	s_add_u32 s42, s70, 0x4500
	s_addc_u32 s43, s71, 0
	v_rcp_iflag_f32_e32 v5, v5
	v_add_u32_e32 v3, s0, v3
	v_add_u32_e32 v6, 1, v3
	s_mov_b64 s[44:45], -1
	v_mul_f32_e32 v4, 0x4f7ffffe, v5
	v_cvt_u32_f32_e32 v4, v4
	v_sub_u32_e32 v5, 0, v2
	v_mul_lo_u32 v5, v5, v4
	v_mul_hi_u32 v5, v4, v5
	v_add_u32_e32 v4, v4, v5
	v_mul_hi_u32 v4, v3, v4
	v_mul_lo_u32 v5, v4, v2
	v_sub_u32_e32 v3, v3, v5
	v_add_u32_e32 v7, 1, v4
	v_cmp_ge_u32_e32 vcc, v3, v2
	v_sub_u32_e32 v5, v3, v2
	s_nop 0
	v_cndmask_b32_e32 v4, v4, v7, vcc
	v_cndmask_b32_e32 v3, v3, v5, vcc
	v_add_u32_e32 v5, 1, v4
	v_cmp_ge_u32_e32 vcc, v3, v2
	s_nop 1
	v_cndmask_b32_e32 v4, v4, v5, vcc
	v_mul_lo_u32 v3, v2, v4
	v_add_u32_e32 v2, v3, v2
	v_cmp_ne_u32_e32 vcc, v6, v2
	v_mov_b32_e32 v6, v2
	v_mov_b64_e32 v[2:3], s[42:43]
	s_and_saveexec_b64 s[40:41], vcc
	s_cbranch_execz .LBB0_777
	v_mov_b32_e32 v2, 0
	global_load_dword v3, v2, s[42:43] offset:-256 sc1
	s_mov_b64 s[48:49], 0
	s_waitcnt vmcnt(0)
	v_cmp_lt_u32_e32 vcc, v3, v6
	s_and_saveexec_b64 s[46:47], vcc
	s_cbranch_execz .LBB0_776
	s_add_u32 s44, s70, 0x1200
	s_addc_u32 s45, s71, 0
	s_mov_b32 s0, 1
	s_branch .LBB0_769

; __device__ __forceinline__ unsigned xb_ld(unsigned* p)              { return __hip_atomic_load(p, __ATOMIC_RELAXED, __HIP_MEMORY_SCOPE_AGENT); }
; #define XB_SPIN(cond, bar) do { unsigned _sp = 0; while (cond) { __builtin_amdgcn_s_sleep(1); \
;     if ((++_sp & 255u) == 0u) { if (xb_ld(&(bar)[XB_TMO])) break; if (_sp > XB_SPIN_CAP) { atomicAdd(&(bar)[XB_TMO], 1u); break; } } } } while (0)
; __device__ __forceinline__ void xcd_barrier(const XcdBarrier& b) {
;     ...
;             else XB_SPIN(xb_ld(&bar[XB_TOPGEN]) == tg, bar);
.LBB0_771:
	global_load_dword v3, v2, s[42:43] offset:-256 sc1
	s_add_i32 s0, s0, 1
	s_mov_b64 s[52:53], -1
	s_waitcnt vmcnt(0)
	v_cmp_ge_u32_e32 vcc, v3, v6
	s_orn2_b64 s[56:57], vcc, exec
	s_branch .LBB0_768

; __device__ __forceinline__ unsigned xb_ld(unsigned* p)              { return __hip_atomic_load(p, __ATOMIC_RELAXED, __HIP_MEMORY_SCOPE_AGENT); }
; __device__ __forceinline__ unsigned xb_add(unsigned* p, unsigned v) { return __hip_atomic_fetch_add(p, v, __ATOMIC_RELAXED, __HIP_MEMORY_SCOPE_AGENT); }
; #define XB_SPIN(cond, bar) do { unsigned _sp = 0; while (cond) { __builtin_amdgcn_s_sleep(1); \
;     if ((++_sp & 255u) == 0u) { if (xb_ld(&(bar)[XB_TMO])) break; if (_sp > XB_SPIN_CAP) { atomicAdd(&(bar)[XB_TMO], 1u); break; } } } } while (0)
; __device__ __forceinline__ void xcd_barrier(const XcdBarrier& b) {
;     ...
;         const unsigned old = xb_add(&bar[XB_XSUB(b.x)], 1u);
;         const unsigned gen = old / nloc;
;         if (old + 1u == (gen + 1u) * nloc) {
;             __builtin_amdgcn_fence(__ATOMIC_RELEASE, "agent");
;             asm volatile("s_waitcnt vmcnt(0)" ::: "memory");
;             const unsigned og = xb_add(&bar[XB_TOP], 1u);
;             const unsigned tg = og / nx;
;             if (og + 1u == (tg + 1u) * nx) xb_add(&bar[XB_TOPGEN], 1u);
;             else XB_SPIN(xb_ld(&bar[XB_TOPGEN]) == tg, bar);
;             xb_add(&bar[XB_XGEN(b.x)], 1u);
;             __builtin_amdgcn_fence(__ATOMIC_ACQUIRE, "agent");
;         } else {
;             XB_SPIN(xb_ld(&bar[XB_XGEN(b.x)]) == gen, bar);
.LBB0_839:
	s_or_b64 exec, exec, s[22:23]
	v_cvt_f32_u32_e32 v6, v4
	s_waitcnt vmcnt(0)
	v_readfirstlane_b32 s0, v5
	v_sub_u32_e32 v5, 0, v4
	v_rcp_iflag_f32_e32 v6, v6
	v_add_u32_e32 v7, s0, v3
	v_mul_f32_e32 v6, 0x4f7ffffe, v6
	v_cvt_u32_f32_e32 v6, v6
	v_mul_lo_u32 v3, v5, v6
	v_mul_hi_u32 v3, v6, v3
	v_add_u32_e32 v3, v6, v3
	v_mul_hi_u32 v3, v7, v3
	v_mul_lo_u32 v5, v3, v4
	v_sub_u32_e32 v5, v7, v5
	v_add_u32_e32 v6, 1, v3
	v_cmp_ge_u32_e32 vcc, v5, v4
	s_nop 1
	v_cndmask_b32_e32 v3, v3, v6, vcc
	v_sub_u32_e32 v6, v5, v4
	v_cndmask_b32_e32 v5, v5, v6, vcc
	v_add_u32_e32 v6, 1, v3
	v_cmp_ge_u32_e32 vcc, v5, v4
	v_add_u32_e32 v5, 1, v7
	s_nop 0
	v_cndmask_b32_e32 v3, v3, v6, vcc
	v_mul_lo_u32 v6, v4, v3
	v_add_u32_e32 v4, v6, v4
	v_cmp_ne_u32_e32 vcc, v5, v4
	s_and_saveexec_b64 s[0:1], vcc
	s_xor_b64 s[14:15], exec, s[0:1]
	s_cbranch_execz .LBB0_853
	s_waitcnt lgkmcnt(0)
	v_mad_u32_u24 v5, v3, v2, v2
	v_mov_b32_e32 v2, 0x4000
	global_load_dword v2, v2, s[70:71] offset:1024 sc1
	s_add_u32 s40, s70, 0x4400
	s_addc_u32 s41, s71, 0
	s_waitcnt vmcnt(0)
	v_cmp_lt_u32_e32 vcc, v2, v5
	s_and_saveexec_b64 s[22:23], vcc
	s_cbranch_execz .LBB0_852
	s_add_u32 s38, s70, 0x1200
	s_addc_u32 s39, s71, 0
	s_mov_b32 s0, 1
	s_mov_b64 s[42:43], 0
	v_mov_b32_e32 v2, 0
	s_branch .LBB0_843

; __device__ __forceinline__ unsigned xb_ld(unsigned* p)              { return __hip_atomic_load(p, __ATOMIC_RELAXED, __HIP_MEMORY_SCOPE_AGENT); }
; #define XB_SPIN(cond, bar) do { unsigned _sp = 0; while (cond) { __builtin_amdgcn_s_sleep(1); \
;     if ((++_sp & 255u) == 0u) { if (xb_ld(&(bar)[XB_TMO])) break; if (_sp > XB_SPIN_CAP) { atomicAdd(&(bar)[XB_TMO], 1u); break; } } } } while (0)
; __device__ __forceinline__ void xcd_barrier(const XcdBarrier& b) {
;     ...
;             XB_SPIN(xb_ld(&bar[XB_XGEN(b.x)]) == gen, bar);
.LBB0_845:
	global_load_dword v4, v2, s[40:41] sc1
	s_add_i32 s0, s0, 1
	s_mov_b64 s[48:49], -1
	s_waitcnt vmcnt(0)
	v_cmp_ge_u32_e32 vcc, v4, v5
	s_orn2_b64 s[46:47], vcc, exec
	s_branch .LBB0_842

; __device__ __forceinline__ unsigned xb_ld(unsigned* p)              { return __hip_atomic_load(p, __ATOMIC_RELAXED, __HIP_MEMORY_SCOPE_AGENT); }
; __device__ __forceinline__ unsigned xb_add(unsigned* p, unsigned v) { return __hip_atomic_fetch_add(p, v, __ATOMIC_RELAXED, __HIP_MEMORY_SCOPE_AGENT); }
; #define XB_SPIN(cond, bar) do { unsigned _sp = 0; while (cond) { __builtin_amdgcn_s_sleep(1); \
;     if ((++_sp & 255u) == 0u) { if (xb_ld(&(bar)[XB_TMO])) break; if (_sp > XB_SPIN_CAP) { atomicAdd(&(bar)[XB_TMO], 1u); break; } } } } while (0)
; __device__ __forceinline__ void xcd_barrier(const XcdBarrier& b) {
;     ...
;         if (old + 1u == (gen + 1u) * nloc) {
;             __builtin_amdgcn_fence(__ATOMIC_RELEASE, "agent");
;             asm volatile("s_waitcnt vmcnt(0)" ::: "memory");
;             const unsigned og = xb_add(&bar[XB_TOP], 1u);
;             const unsigned tg = og / nx;
;             if (og + 1u == (tg + 1u) * nx) xb_add(&bar[XB_TOPGEN], 1u);
;             else XB_SPIN(xb_ld(&bar[XB_TOPGEN]) == tg, bar);
.LBB0_856:
	s_or_b64 exec, exec, s[38:39]
	v_cvt_f32_u32_e32 v5, v2
	s_waitcnt vmcnt(0)
	v_readfirstlane_b32 s0, v4
	s_add_u32 s38, s70, 0x4500
	s_addc_u32 s39, s71, 0
	v_rcp_iflag_f32_e32 v5, v5
	v_add_u32_e32 v3, s0, v3
	v_add_u32_e32 v6, 1, v3
	s_mov_b64 s[40:41], -1
	v_mul_f32_e32 v4, 0x4f7ffffe, v5
	v_cvt_u32_f32_e32 v4, v4
	v_sub_u32_e32 v5, 0, v2
	v_mul_lo_u32 v5, v5, v4
	v_mul_hi_u32 v5, v4, v5
	v_add_u32_e32 v4, v4, v5
	v_mul_hi_u32 v4, v3, v4
	v_mul_lo_u32 v5, v4, v2
	v_sub_u32_e32 v3, v3, v5
	v_add_u32_e32 v7, 1, v4
	v_cmp_ge_u32_e32 vcc, v3, v2
	v_sub_u32_e32 v5, v3, v2
	s_nop 0
	v_cndmask_b32_e32 v4, v4, v7, vcc
	v_cndmask_b32_e32 v3, v3, v5, vcc
	v_add_u32_e32 v5, 1, v4
	v_cmp_ge_u32_e32 vcc, v3, v2
	s_nop 1
	v_cndmask_b32_e32 v4, v4, v5, vcc
	v_mul_lo_u32 v3, v2, v4
	v_add_u32_e32 v2, v3, v2
	v_cmp_ne_u32_e32 vcc, v6, v2
	v_mov_b32_e32 v6, v2
	v_mov_b64_e32 v[2:3], s[38:39]
	s_and_saveexec_b64 s[22:23], vcc
	s_cbranch_execz .LBB0_868
	v_mov_b32_e32 v2, 0
	global_load_dword v3, v2, s[38:39] offset:-256 sc1
	s_mov_b64 s[44:45], 0
	s_waitcnt vmcnt(0)
	v_cmp_lt_u32_e32 vcc, v3, v6
	s_and_saveexec_b64 s[42:43], vcc
	s_cbranch_execz .LBB0_867
	s_add_u32 s40, s70, 0x1200
	s_addc_u32 s41, s71, 0
	s_mov_b32 s0, 1
	s_branch .LBB0_860

; __device__ __forceinline__ unsigned xb_ld(unsigned* p)              { return __hip_atomic_load(p, __ATOMIC_RELAXED, __HIP_MEMORY_SCOPE_AGENT); }
; #define XB_SPIN(cond, bar) do { unsigned _sp = 0; while (cond) { __builtin_amdgcn_s_sleep(1); \
;     if ((++_sp & 255u) == 0u) { if (xb_ld(&(bar)[XB_TMO])) break; if (_sp > XB_SPIN_CAP) { atomicAdd(&(bar)[XB_TMO], 1u); break; } } } } while (0)
; __device__ __forceinline__ void xcd_barrier(const XcdBarrier& b) {
;     ...
;             else XB_SPIN(xb_ld(&bar[XB_TOPGEN]) == tg, bar);
.LBB0_862:
	global_load_dword v3, v2, s[38:39] offset:-256 sc1
	s_add_i32 s0, s0, 1
	s_mov_b64 s[48:49], -1
	s_waitcnt vmcnt(0)
	v_cmp_ge_u32_e32 vcc, v3, v6
	s_orn2_b64 s[52:53], vcc, exec
	s_branch .LBB0_859

; __device__ __forceinline__ unsigned xb_ld(unsigned* p)              { return __hip_atomic_load(p, __ATOMIC_RELAXED, __HIP_MEMORY_SCOPE_AGENT); }
; __device__ __forceinline__ unsigned xb_add(unsigned* p, unsigned v) { return __hip_atomic_fetch_add(p, v, __ATOMIC_RELAXED, __HIP_MEMORY_SCOPE_AGENT); }
; #define XB_SPIN(cond, bar) do { unsigned _sp = 0; while (cond) { __builtin_amdgcn_s_sleep(1); \
;     if ((++_sp & 255u) == 0u) { if (xb_ld(&(bar)[XB_TMO])) break; if (_sp > XB_SPIN_CAP) { atomicAdd(&(bar)[XB_TMO], 1u); break; } } } } while (0)
; __device__ __forceinline__ void xcd_barrier(const XcdBarrier& b) {
;     ...
;         const unsigned old = xb_add(&bar[XB_XSUB(b.x)], 1u);
;         const unsigned gen = old / nloc;
;         if (old + 1u == (gen + 1u) * nloc) {
;             __builtin_amdgcn_fence(__ATOMIC_RELEASE, "agent");
;             asm volatile("s_waitcnt vmcnt(0)" ::: "memory");
;             const unsigned og = xb_add(&bar[XB_TOP], 1u);
;             const unsigned tg = og / nx;
;             if (og + 1u == (tg + 1u) * nx) xb_add(&bar[XB_TOPGEN], 1u);
;             else XB_SPIN(xb_ld(&bar[XB_TOPGEN]) == tg, bar);
;             xb_add(&bar[XB_XGEN(b.x)], 1u);
;             __builtin_amdgcn_fence(__ATOMIC_ACQUIRE, "agent");
;         } else {
;             XB_SPIN(xb_ld(&bar[XB_XGEN(b.x)]) == gen, bar);
.LBB0_897:
	s_or_b64 exec, exec, s[12:13]
	v_cvt_f32_u32_e32 v6, v4
	s_waitcnt vmcnt(0)
	v_readfirstlane_b32 s0, v5
	v_sub_u32_e32 v5, 0, v4
	v_rcp_iflag_f32_e32 v6, v6
	v_add_u32_e32 v7, s0, v3
	v_mul_f32_e32 v6, 0x4f7ffffe, v6
	v_cvt_u32_f32_e32 v6, v6
	v_mul_lo_u32 v3, v5, v6
	v_mul_hi_u32 v3, v6, v3
	v_add_u32_e32 v3, v6, v3
	v_mul_hi_u32 v3, v7, v3
	v_mul_lo_u32 v5, v3, v4
	v_sub_u32_e32 v5, v7, v5
	v_add_u32_e32 v6, 1, v3
	v_cmp_ge_u32_e32 vcc, v5, v4
	s_nop 1
	v_cndmask_b32_e32 v3, v3, v6, vcc
	v_sub_u32_e32 v6, v5, v4
	v_cndmask_b32_e32 v5, v5, v6, vcc
	v_add_u32_e32 v6, 1, v3
	v_cmp_ge_u32_e32 vcc, v5, v4
	v_add_u32_e32 v5, 1, v7
	s_nop 0
	v_cndmask_b32_e32 v3, v3, v6, vcc
	v_mul_lo_u32 v6, v4, v3
	v_add_u32_e32 v4, v6, v4
	v_cmp_ne_u32_e32 vcc, v5, v4
	s_and_saveexec_b64 s[0:1], vcc
	s_xor_b64 s[8:9], exec, s[0:1]
	s_cbranch_execz .LBB0_911
	s_waitcnt lgkmcnt(0)
	v_mad_u32_u24 v5, v3, v2, v2
	v_mov_b32_e32 v2, 0x4000
	global_load_dword v2, v2, s[70:71] offset:1024 sc1
	s_add_u32 s22, s70, 0x4400
	s_addc_u32 s23, s71, 0
	s_waitcnt vmcnt(0)
	v_cmp_lt_u32_e32 vcc, v2, v5
	s_and_saveexec_b64 s[12:13], vcc
	s_cbranch_execz .LBB0_910
	s_add_u32 s14, s70, 0x1200
	s_addc_u32 s15, s71, 0
	s_mov_b32 s0, 1
	s_mov_b64 s[30:31], 0
	v_mov_b32_e32 v2, 0
	s_branch .LBB0_901

; __device__ __forceinline__ unsigned xb_ld(unsigned* p)              { return __hip_atomic_load(p, __ATOMIC_RELAXED, __HIP_MEMORY_SCOPE_AGENT); }
; #define XB_SPIN(cond, bar) do { unsigned _sp = 0; while (cond) { __builtin_amdgcn_s_sleep(1); \
;     if ((++_sp & 255u) == 0u) { if (xb_ld(&(bar)[XB_TMO])) break; if (_sp > XB_SPIN_CAP) { atomicAdd(&(bar)[XB_TMO], 1u); break; } } } } while (0)
; __device__ __forceinline__ void xcd_barrier(const XcdBarrier& b) {
;     ...
;             XB_SPIN(xb_ld(&bar[XB_XGEN(b.x)]) == gen, bar);
.LBB0_903:
	global_load_dword v4, v2, s[22:23] sc1
	s_add_i32 s0, s0, 1
	s_mov_b64 s[42:43], -1
	s_waitcnt vmcnt(0)
	v_cmp_ge_u32_e32 vcc, v4, v5
	s_orn2_b64 s[40:41], vcc, exec
	s_branch .LBB0_900

; __device__ __forceinline__ unsigned xb_ld(unsigned* p)              { return __hip_atomic_load(p, __ATOMIC_RELAXED, __HIP_MEMORY_SCOPE_AGENT); }
; __device__ __forceinline__ unsigned xb_add(unsigned* p, unsigned v) { return __hip_atomic_fetch_add(p, v, __ATOMIC_RELAXED, __HIP_MEMORY_SCOPE_AGENT); }
; #define XB_SPIN(cond, bar) do { unsigned _sp = 0; while (cond) { __builtin_amdgcn_s_sleep(1); \
;     if ((++_sp & 255u) == 0u) { if (xb_ld(&(bar)[XB_TMO])) break; if (_sp > XB_SPIN_CAP) { atomicAdd(&(bar)[XB_TMO], 1u); break; } } } } while (0)
; __device__ __forceinline__ void xcd_barrier(const XcdBarrier& b) {
;     ...
;         if (old + 1u == (gen + 1u) * nloc) {
;             __builtin_amdgcn_fence(__ATOMIC_RELEASE, "agent");
;             asm volatile("s_waitcnt vmcnt(0)" ::: "memory");
;             const unsigned og = xb_add(&bar[XB_TOP], 1u);
;             const unsigned tg = og / nx;
;             if (og + 1u == (tg + 1u) * nx) xb_add(&bar[XB_TOPGEN], 1u);
;             else XB_SPIN(xb_ld(&bar[XB_TOPGEN]) == tg, bar);
.LBB0_914:
	s_or_b64 exec, exec, s[12:13]
	v_cvt_f32_u32_e32 v5, v2
	s_waitcnt vmcnt(0)
	v_readfirstlane_b32 s0, v4
	s_add_u32 s12, s70, 0x4500
	s_addc_u32 s13, s71, 0
	v_rcp_iflag_f32_e32 v5, v5
	v_add_u32_e32 v3, s0, v3
	v_add_u32_e32 v6, 1, v3
	s_mov_b64 s[14:15], -1
	v_mul_f32_e32 v4, 0x4f7ffffe, v5
	v_cvt_u32_f32_e32 v4, v4
	v_sub_u32_e32 v5, 0, v2
	v_mul_lo_u32 v5, v5, v4
	v_mul_hi_u32 v5, v4, v5
	v_add_u32_e32 v4, v4, v5
	v_mul_hi_u32 v4, v3, v4
	v_mul_lo_u32 v5, v4, v2
	v_sub_u32_e32 v3, v3, v5
	v_add_u32_e32 v7, 1, v4
	v_cmp_ge_u32_e32 vcc, v3, v2
	v_sub_u32_e32 v5, v3, v2
	s_nop 0
	v_cndmask_b32_e32 v4, v4, v7, vcc
	v_cndmask_b32_e32 v3, v3, v5, vcc
	v_add_u32_e32 v5, 1, v4
	v_cmp_ge_u32_e32 vcc, v3, v2
	s_nop 1
	v_cndmask_b32_e32 v4, v4, v5, vcc
	v_mul_lo_u32 v3, v2, v4
	v_add_u32_e32 v2, v3, v2
	v_cmp_ne_u32_e32 vcc, v6, v2
	v_mov_b32_e32 v6, v2
	v_mov_b64_e32 v[2:3], s[12:13]
	s_and_saveexec_b64 s[8:9], vcc
	s_cbranch_execz .LBB0_926
	v_mov_b32_e32 v2, 0
	global_load_dword v3, v2, s[12:13] offset:-256 sc1
	s_mov_b64 s[30:31], 0
	s_waitcnt vmcnt(0)
	v_cmp_lt_u32_e32 vcc, v3, v6
	s_and_saveexec_b64 s[22:23], vcc
	s_cbranch_execz .LBB0_925
	s_add_u32 s14, s70, 0x1200
	s_addc_u32 s15, s71, 0
	s_mov_b32 s0, 1
	s_branch .LBB0_918

; __device__ __forceinline__ unsigned xb_ld(unsigned* p)              { return __hip_atomic_load(p, __ATOMIC_RELAXED, __HIP_MEMORY_SCOPE_AGENT); }
; #define XB_SPIN(cond, bar) do { unsigned _sp = 0; while (cond) { __builtin_amdgcn_s_sleep(1); \
;     if ((++_sp & 255u) == 0u) { if (xb_ld(&(bar)[XB_TMO])) break; if (_sp > XB_SPIN_CAP) { atomicAdd(&(bar)[XB_TMO], 1u); break; } } } } while (0)
; __device__ __forceinline__ void xcd_barrier(const XcdBarrier& b) {
;     ...
;             else XB_SPIN(xb_ld(&bar[XB_TOPGEN]) == tg, bar);
.LBB0_920:
	global_load_dword v3, v2, s[12:13] offset:-256 sc1
	s_add_i32 s0, s0, 1
	s_mov_b64 s[40:41], -1
	s_waitcnt vmcnt(0)
	v_cmp_ge_u32_e32 vcc, v3, v6
	s_orn2_b64 s[44:45], vcc, exec
	s_branch .LBB0_917

; __device__ __forceinline__ unsigned xb_ld(unsigned* p)              { return __hip_atomic_load(p, __ATOMIC_RELAXED, __HIP_MEMORY_SCOPE_AGENT); }
; __device__ __forceinline__ unsigned xb_add(unsigned* p, unsigned v) { return __hip_atomic_fetch_add(p, v, __ATOMIC_RELAXED, __HIP_MEMORY_SCOPE_AGENT); }
; #define XB_SPIN(cond, bar) do { unsigned _sp = 0; while (cond) { __builtin_amdgcn_s_sleep(1); \
;     if ((++_sp & 255u) == 0u) { if (xb_ld(&(bar)[XB_TMO])) break; if (_sp > XB_SPIN_CAP) { atomicAdd(&(bar)[XB_TMO], 1u); break; } } } } while (0)
; __device__ __forceinline__ void xcd_barrier(const XcdBarrier& b) {
;     ...
;         const unsigned old = xb_add(&bar[XB_XSUB(b.x)], 1u);
;         const unsigned gen = old / nloc;
;         if (old + 1u == (gen + 1u) * nloc) {
;             __builtin_amdgcn_fence(__ATOMIC_RELEASE, "agent");
;             asm volatile("s_waitcnt vmcnt(0)" ::: "memory");
;             const unsigned og = xb_add(&bar[XB_TOP], 1u);
;             const unsigned tg = og / nx;
;             if (og + 1u == (tg + 1u) * nx) xb_add(&bar[XB_TOPGEN], 1u);
;             else XB_SPIN(xb_ld(&bar[XB_TOPGEN]) == tg, bar);
;             xb_add(&bar[XB_XGEN(b.x)], 1u);
;             __builtin_amdgcn_fence(__ATOMIC_ACQUIRE, "agent");
;         } else {
;             XB_SPIN(xb_ld(&bar[XB_XGEN(b.x)]) == gen, bar);
.LBB0_985:
	s_or_b64 exec, exec, s[14:15]
	v_cvt_f32_u32_e32 v6, v4
	s_waitcnt vmcnt(0)
	v_readfirstlane_b32 s0, v5
	v_sub_u32_e32 v5, 0, v4
	v_rcp_iflag_f32_e32 v6, v6
	v_add_u32_e32 v7, s0, v3
	v_mul_f32_e32 v6, 0x4f7ffffe, v6
	v_cvt_u32_f32_e32 v6, v6
	v_mul_lo_u32 v3, v5, v6
	v_mul_hi_u32 v3, v6, v3
	v_add_u32_e32 v3, v6, v3
	v_mul_hi_u32 v3, v7, v3
	v_mul_lo_u32 v5, v3, v4
	v_sub_u32_e32 v5, v7, v5
	v_add_u32_e32 v6, 1, v3
	v_cmp_ge_u32_e32 vcc, v5, v4
	s_nop 1
	v_cndmask_b32_e32 v3, v3, v6, vcc
	v_sub_u32_e32 v6, v5, v4
	v_cndmask_b32_e32 v5, v5, v6, vcc
	v_add_u32_e32 v6, 1, v3
	v_cmp_ge_u32_e32 vcc, v5, v4
	v_add_u32_e32 v5, 1, v7
	s_nop 0
	v_cndmask_b32_e32 v3, v3, v6, vcc
	v_mul_lo_u32 v6, v4, v3
	v_add_u32_e32 v4, v6, v4
	v_cmp_ne_u32_e32 vcc, v5, v4
	s_and_saveexec_b64 s[0:1], vcc
	s_xor_b64 s[10:11], exec, s[0:1]
	s_cbranch_execz .LBB0_999
	s_waitcnt lgkmcnt(0)
	v_mad_u32_u24 v5, v3, v2, v2
	v_mov_b32_e32 v2, 0x4000
	global_load_dword v2, v2, s[70:71] offset:1024 sc1
	s_add_u32 s30, s70, 0x4400
	s_addc_u32 s31, s71, 0
	s_waitcnt vmcnt(0)
	v_cmp_lt_u32_e32 vcc, v2, v5
	s_and_saveexec_b64 s[14:15], vcc
	s_cbranch_execz .LBB0_998
	s_add_u32 s22, s70, 0x1200
	s_addc_u32 s23, s71, 0
	s_mov_b32 s0, 1
	s_mov_b64 s[38:39], 0
	v_mov_b32_e32 v2, 0
	s_branch .LBB0_989

; __device__ __forceinline__ unsigned xb_ld(unsigned* p)              { return __hip_atomic_load(p, __ATOMIC_RELAXED, __HIP_MEMORY_SCOPE_AGENT); }
; #define XB_SPIN(cond, bar) do { unsigned _sp = 0; while (cond) { __builtin_amdgcn_s_sleep(1); \
;     if ((++_sp & 255u) == 0u) { if (xb_ld(&(bar)[XB_TMO])) break; if (_sp > XB_SPIN_CAP) { atomicAdd(&(bar)[XB_TMO], 1u); break; } } } } while (0)
; __device__ __forceinline__ void xcd_barrier(const XcdBarrier& b) {
;     ...
;             XB_SPIN(xb_ld(&bar[XB_XGEN(b.x)]) == gen, bar);
.LBB0_991:
	global_load_dword v4, v2, s[30:31] sc1
	s_add_i32 s0, s0, 1
	s_mov_b64 s[44:45], -1
	s_waitcnt vmcnt(0)
	v_cmp_ge_u32_e32 vcc, v4, v5
	s_orn2_b64 s[42:43], vcc, exec
	s_branch .LBB0_988

; __device__ __forceinline__ unsigned xb_ld(unsigned* p)              { return __hip_atomic_load(p, __ATOMIC_RELAXED, __HIP_MEMORY_SCOPE_AGENT); }
; __device__ __forceinline__ unsigned xb_add(unsigned* p, unsigned v) { return __hip_atomic_fetch_add(p, v, __ATOMIC_RELAXED, __HIP_MEMORY_SCOPE_AGENT); }
; #define XB_SPIN(cond, bar) do { unsigned _sp = 0; while (cond) { __builtin_amdgcn_s_sleep(1); \
;     if ((++_sp & 255u) == 0u) { if (xb_ld(&(bar)[XB_TMO])) break; if (_sp > XB_SPIN_CAP) { atomicAdd(&(bar)[XB_TMO], 1u); break; } } } } while (0)
; __device__ __forceinline__ void xcd_barrier(const XcdBarrier& b) {
;     ...
;         if (old + 1u == (gen + 1u) * nloc) {
;             __builtin_amdgcn_fence(__ATOMIC_RELEASE, "agent");
;             asm volatile("s_waitcnt vmcnt(0)" ::: "memory");
;             const unsigned og = xb_add(&bar[XB_TOP], 1u);
;             const unsigned tg = og / nx;
;             if (og + 1u == (tg + 1u) * nx) xb_add(&bar[XB_TOPGEN], 1u);
;             else XB_SPIN(xb_ld(&bar[XB_TOPGEN]) == tg, bar);
.LBB0_1002:
	s_or_b64 exec, exec, s[22:23]
	v_cvt_f32_u32_e32 v5, v2
	s_waitcnt vmcnt(0)
	v_readfirstlane_b32 s0, v4
	s_add_u32 s22, s70, 0x4500
	s_addc_u32 s23, s71, 0
	v_rcp_iflag_f32_e32 v5, v5
	v_add_u32_e32 v3, s0, v3
	v_add_u32_e32 v6, 1, v3
	s_mov_b64 s[30:31], -1
	v_mul_f32_e32 v4, 0x4f7ffffe, v5
	v_cvt_u32_f32_e32 v4, v4
	v_sub_u32_e32 v5, 0, v2
	v_mul_lo_u32 v5, v5, v4
	v_mul_hi_u32 v5, v4, v5
	v_add_u32_e32 v4, v4, v5
	v_mul_hi_u32 v4, v3, v4
	v_mul_lo_u32 v5, v4, v2
	v_sub_u32_e32 v3, v3, v5
	v_add_u32_e32 v7, 1, v4
	v_cmp_ge_u32_e32 vcc, v3, v2
	v_sub_u32_e32 v5, v3, v2
	s_nop 0
	v_cndmask_b32_e32 v4, v4, v7, vcc
	v_cndmask_b32_e32 v3, v3, v5, vcc
	v_add_u32_e32 v5, 1, v4
	v_cmp_ge_u32_e32 vcc, v3, v2
	s_nop 1
	v_cndmask_b32_e32 v4, v4, v5, vcc
	v_mul_lo_u32 v3, v2, v4
	v_add_u32_e32 v2, v3, v2
	v_cmp_ne_u32_e32 vcc, v6, v2
	v_mov_b32_e32 v6, v2
	v_mov_b64_e32 v[2:3], s[22:23]
	s_and_saveexec_b64 s[14:15], vcc
	s_cbranch_execz .LBB0_1014
	v_mov_b32_e32 v2, 0
	global_load_dword v3, v2, s[22:23] offset:-256 sc1
	s_mov_b64 s[40:41], 0
	s_waitcnt vmcnt(0)
	v_cmp_lt_u32_e32 vcc, v3, v6
	s_and_saveexec_b64 s[38:39], vcc
	s_cbranch_execz .LBB0_1013
	s_add_u32 s30, s70, 0x1200
	s_addc_u32 s31, s71, 0
	s_mov_b32 s0, 1
	s_branch .LBB0_1006

; __device__ __forceinline__ unsigned xb_ld(unsigned* p)              { return __hip_atomic_load(p, __ATOMIC_RELAXED, __HIP_MEMORY_SCOPE_AGENT); }
; #define XB_SPIN(cond, bar) do { unsigned _sp = 0; while (cond) { __builtin_amdgcn_s_sleep(1); \
;     if ((++_sp & 255u) == 0u) { if (xb_ld(&(bar)[XB_TMO])) break; if (_sp > XB_SPIN_CAP) { atomicAdd(&(bar)[XB_TMO], 1u); break; } } } } while (0)
; __device__ __forceinline__ void xcd_barrier(const XcdBarrier& b) {
;     ...
;             else XB_SPIN(xb_ld(&bar[XB_TOPGEN]) == tg, bar);
.LBB0_1008:
	global_load_dword v3, v2, s[22:23] offset:-256 sc1
	s_add_i32 s0, s0, 1
	s_mov_b64 s[44:45], -1
	s_waitcnt vmcnt(0)
	v_cmp_ge_u32_e32 vcc, v3, v6
	s_orn2_b64 s[48:49], vcc, exec
	s_branch .LBB0_1005

; __device__ __forceinline__ unsigned xb_ld(unsigned* p)              { return __hip_atomic_load(p, __ATOMIC_RELAXED, __HIP_MEMORY_SCOPE_AGENT); }
; __device__ __forceinline__ unsigned xb_add(unsigned* p, unsigned v) { return __hip_atomic_fetch_add(p, v, __ATOMIC_RELAXED, __HIP_MEMORY_SCOPE_AGENT); }
; #define XB_SPIN(cond, bar) do { unsigned _sp = 0; while (cond) { __builtin_amdgcn_s_sleep(1); \
;     if ((++_sp & 255u) == 0u) { if (xb_ld(&(bar)[XB_TMO])) break; if (_sp > XB_SPIN_CAP) { atomicAdd(&(bar)[XB_TMO], 1u); break; } } } } while (0)
; __device__ __forceinline__ void xcd_barrier(const XcdBarrier& b) {
;     ...
;         const unsigned old = xb_add(&bar[XB_XSUB(b.x)], 1u);
;         const unsigned gen = old / nloc;
;         if (old + 1u == (gen + 1u) * nloc) {
;             __builtin_amdgcn_fence(__ATOMIC_RELEASE, "agent");
;             asm volatile("s_waitcnt vmcnt(0)" ::: "memory");
;             const unsigned og = xb_add(&bar[XB_TOP], 1u);
;             const unsigned tg = og / nx;
;             if (og + 1u == (tg + 1u) * nx) xb_add(&bar[XB_TOPGEN], 1u);
;             else XB_SPIN(xb_ld(&bar[XB_TOPGEN]) == tg, bar);
;             xb_add(&bar[XB_XGEN(b.x)], 1u);
;             __builtin_amdgcn_fence(__ATOMIC_ACQUIRE, "agent");
;         } else {
;             XB_SPIN(xb_ld(&bar[XB_XGEN(b.x)]) == gen, bar);
.LBB0_1074:
	s_or_b64 exec, exec, s[12:13]
	v_cvt_f32_u32_e32 v6, v4
	s_waitcnt vmcnt(0)
	v_readfirstlane_b32 s10, v5
	v_sub_u32_e32 v5, 0, v4
	v_rcp_iflag_f32_e32 v6, v6
	v_add_u32_e32 v7, s10, v3
	v_mul_f32_e32 v6, 0x4f7ffffe, v6
	v_cvt_u32_f32_e32 v6, v6
	v_mul_lo_u32 v3, v5, v6
	v_mul_hi_u32 v3, v6, v3
	v_add_u32_e32 v3, v6, v3
	v_mul_hi_u32 v3, v7, v3
	v_mul_lo_u32 v5, v3, v4
	v_sub_u32_e32 v5, v7, v5
	v_add_u32_e32 v6, 1, v3
	v_cmp_ge_u32_e32 vcc, v5, v4
	s_nop 1
	v_cndmask_b32_e32 v3, v3, v6, vcc
	v_sub_u32_e32 v6, v5, v4
	v_cndmask_b32_e32 v5, v5, v6, vcc
	v_add_u32_e32 v6, 1, v3
	v_cmp_ge_u32_e32 vcc, v5, v4
	v_add_u32_e32 v5, 1, v7
	s_nop 0
	v_cndmask_b32_e32 v3, v3, v6, vcc
	v_mul_lo_u32 v6, v4, v3
	v_add_u32_e32 v4, v6, v4
	v_cmp_ne_u32_e32 vcc, v5, v4
	s_and_saveexec_b64 s[10:11], vcc
	s_xor_b64 s[10:11], exec, s[10:11]
	s_cbranch_execz .LBB0_1088
	s_waitcnt lgkmcnt(0)
	v_mad_u32_u24 v5, v3, v2, v2
	v_mov_b32_e32 v2, 0x4000
	global_load_dword v2, v2, s[70:71] offset:1024 sc1
	s_add_u32 s22, s70, 0x4400
	s_addc_u32 s23, s71, 0
	s_waitcnt vmcnt(0)
	v_cmp_lt_u32_e32 vcc, v2, v5
	s_and_saveexec_b64 s[12:13], vcc
	s_cbranch_execz .LBB0_1087
	s_add_u32 s14, s70, 0x1200
	s_addc_u32 s15, s71, 0
	s_mov_b32 s18, 1
	s_mov_b64 s[26:27], 0
	v_mov_b32_e32 v2, 0
	s_branch .LBB0_1078

; __device__ __forceinline__ unsigned xb_ld(unsigned* p)              { return __hip_atomic_load(p, __ATOMIC_RELAXED, __HIP_MEMORY_SCOPE_AGENT); }
; #define XB_SPIN(cond, bar) do { unsigned _sp = 0; while (cond) { __builtin_amdgcn_s_sleep(1); \
;     if ((++_sp & 255u) == 0u) { if (xb_ld(&(bar)[XB_TMO])) break; if (_sp > XB_SPIN_CAP) { atomicAdd(&(bar)[XB_TMO], 1u); break; } } } } while (0)
; __device__ __forceinline__ void xcd_barrier(const XcdBarrier& b) {
;     ...
;             XB_SPIN(xb_ld(&bar[XB_XGEN(b.x)]) == gen, bar);
.LBB0_1080:
	global_load_dword v4, v2, s[22:23] sc1
	s_add_i32 s18, s18, 1
	s_mov_b64 s[42:43], -1
	s_waitcnt vmcnt(0)
	v_cmp_ge_u32_e32 vcc, v4, v5
	s_orn2_b64 s[40:41], vcc, exec
	s_branch .LBB0_1077

; __device__ __forceinline__ unsigned xb_ld(unsigned* p)              { return __hip_atomic_load(p, __ATOMIC_RELAXED, __HIP_MEMORY_SCOPE_AGENT); }
; __device__ __forceinline__ unsigned xb_add(unsigned* p, unsigned v) { return __hip_atomic_fetch_add(p, v, __ATOMIC_RELAXED, __HIP_MEMORY_SCOPE_AGENT); }
; #define XB_SPIN(cond, bar) do { unsigned _sp = 0; while (cond) { __builtin_amdgcn_s_sleep(1); \
;     if ((++_sp & 255u) == 0u) { if (xb_ld(&(bar)[XB_TMO])) break; if (_sp > XB_SPIN_CAP) { atomicAdd(&(bar)[XB_TMO], 1u); break; } } } } while (0)
; __device__ __forceinline__ void xcd_barrier(const XcdBarrier& b) {
;     ...
;         if (old + 1u == (gen + 1u) * nloc) {
;             __builtin_amdgcn_fence(__ATOMIC_RELEASE, "agent");
;             asm volatile("s_waitcnt vmcnt(0)" ::: "memory");
;             const unsigned og = xb_add(&bar[XB_TOP], 1u);
;             const unsigned tg = og / nx;
;             if (og + 1u == (tg + 1u) * nx) xb_add(&bar[XB_TOPGEN], 1u);
;             else XB_SPIN(xb_ld(&bar[XB_TOPGEN]) == tg, bar);
.LBB0_1091:
	s_or_b64 exec, exec, s[12:13]
	v_cvt_f32_u32_e32 v5, v2
	s_waitcnt vmcnt(0)
	v_readfirstlane_b32 s10, v4
	s_add_u32 s12, s70, 0x4500
	s_addc_u32 s13, s71, 0
	v_rcp_iflag_f32_e32 v5, v5
	v_add_u32_e32 v3, s10, v3
	v_add_u32_e32 v6, 1, v3
	s_mov_b64 s[14:15], -1
	v_mul_f32_e32 v4, 0x4f7ffffe, v5
	v_cvt_u32_f32_e32 v4, v4
	v_sub_u32_e32 v5, 0, v2
	v_mul_lo_u32 v5, v5, v4
	v_mul_hi_u32 v5, v4, v5
	v_add_u32_e32 v4, v4, v5
	v_mul_hi_u32 v4, v3, v4
	v_mul_lo_u32 v5, v4, v2
	v_sub_u32_e32 v3, v3, v5
	v_add_u32_e32 v7, 1, v4
	v_cmp_ge_u32_e32 vcc, v3, v2
	v_sub_u32_e32 v5, v3, v2
	s_nop 0
	v_cndmask_b32_e32 v4, v4, v7, vcc
	v_cndmask_b32_e32 v3, v3, v5, vcc
	v_add_u32_e32 v5, 1, v4
	v_cmp_ge_u32_e32 vcc, v3, v2
	s_nop 1
	v_cndmask_b32_e32 v4, v4, v5, vcc
	v_mul_lo_u32 v3, v2, v4
	v_add_u32_e32 v2, v3, v2
	v_cmp_ne_u32_e32 vcc, v6, v2
	v_mov_b32_e32 v6, v2
	v_mov_b64_e32 v[2:3], s[12:13]
	s_and_saveexec_b64 s[10:11], vcc
	s_cbranch_execz .LBB0_1103
	v_mov_b32_e32 v2, 0
	global_load_dword v3, v2, s[12:13] offset:-256 sc1
	s_mov_b64 s[26:27], 0
	s_waitcnt vmcnt(0)
	v_cmp_lt_u32_e32 vcc, v3, v6
	s_and_saveexec_b64 s[22:23], vcc
	s_cbranch_execz .LBB0_1102
	s_add_u32 s14, s70, 0x1200
	s_addc_u32 s15, s71, 0
	s_mov_b32 s18, 1
	s_branch .LBB0_1095

; __device__ __forceinline__ unsigned xb_ld(unsigned* p)              { return __hip_atomic_load(p, __ATOMIC_RELAXED, __HIP_MEMORY_SCOPE_AGENT); }
; #define XB_SPIN(cond, bar) do { unsigned _sp = 0; while (cond) { __builtin_amdgcn_s_sleep(1); \
;     if ((++_sp & 255u) == 0u) { if (xb_ld(&(bar)[XB_TMO])) break; if (_sp > XB_SPIN_CAP) { atomicAdd(&(bar)[XB_TMO], 1u); break; } } } } while (0)
; __device__ __forceinline__ void xcd_barrier(const XcdBarrier& b) {
;     ...
;             else XB_SPIN(xb_ld(&bar[XB_TOPGEN]) == tg, bar);
.LBB0_1097:
	global_load_dword v3, v2, s[12:13] offset:-256 sc1
	s_add_i32 s18, s18, 1
	s_mov_b64 s[40:41], -1
	s_waitcnt vmcnt(0)
	v_cmp_ge_u32_e32 vcc, v3, v6
	s_orn2_b64 s[44:45], vcc, exec
	s_branch .LBB0_1094

; __device__ __forceinline__ unsigned xb_ld(unsigned* p)              { return __hip_atomic_load(p, __ATOMIC_RELAXED, __HIP_MEMORY_SCOPE_AGENT); }
; __device__ __forceinline__ unsigned xb_add(unsigned* p, unsigned v) { return __hip_atomic_fetch_add(p, v, __ATOMIC_RELAXED, __HIP_MEMORY_SCOPE_AGENT); }
; #define XB_SPIN(cond, bar) do { unsigned _sp = 0; while (cond) { __builtin_amdgcn_s_sleep(1); \
;     if ((++_sp & 255u) == 0u) { if (xb_ld(&(bar)[XB_TMO])) break; if (_sp > XB_SPIN_CAP) { atomicAdd(&(bar)[XB_TMO], 1u); break; } } } } while (0)
; __device__ __forceinline__ void xcd_barrier(const XcdBarrier& b) {
;     ...
;         const unsigned old = xb_add(&bar[XB_XSUB(b.x)], 1u);
;         const unsigned gen = old / nloc;
;         if (old + 1u == (gen + 1u) * nloc) {
;             __builtin_amdgcn_fence(__ATOMIC_RELEASE, "agent");
;             asm volatile("s_waitcnt vmcnt(0)" ::: "memory");
;             const unsigned og = xb_add(&bar[XB_TOP], 1u);
;             const unsigned tg = og / nx;
;             if (og + 1u == (tg + 1u) * nx) xb_add(&bar[XB_TOPGEN], 1u);
;             else XB_SPIN(xb_ld(&bar[XB_TOPGEN]) == tg, bar);
;             xb_add(&bar[XB_XGEN(b.x)], 1u);
;             __builtin_amdgcn_fence(__ATOMIC_ACQUIRE, "agent");
;         } else {
;             XB_SPIN(xb_ld(&bar[XB_XGEN(b.x)]) == gen, bar);
.LBB0_1146:
	s_or_b64 exec, exec, s[10:11]
	v_cvt_f32_u32_e32 v6, v4
	s_waitcnt vmcnt(0)
	v_readfirstlane_b32 s8, v5
	v_sub_u32_e32 v5, 0, v4
	v_rcp_iflag_f32_e32 v6, v6
	v_add_u32_e32 v7, s8, v3
	v_mul_f32_e32 v6, 0x4f7ffffe, v6
	v_cvt_u32_f32_e32 v6, v6
	v_mul_lo_u32 v3, v5, v6
	v_mul_hi_u32 v3, v6, v3
	v_add_u32_e32 v3, v6, v3
	v_mul_hi_u32 v3, v7, v3
	v_mul_lo_u32 v5, v3, v4
	v_sub_u32_e32 v5, v7, v5
	v_add_u32_e32 v6, 1, v3
	v_cmp_ge_u32_e32 vcc, v5, v4
	s_nop 1
	v_cndmask_b32_e32 v3, v3, v6, vcc
	v_sub_u32_e32 v6, v5, v4
	v_cndmask_b32_e32 v5, v5, v6, vcc
	v_add_u32_e32 v6, 1, v3
	v_cmp_ge_u32_e32 vcc, v5, v4
	v_add_u32_e32 v5, 1, v7
	s_nop 0
	v_cndmask_b32_e32 v3, v3, v6, vcc
	v_mul_lo_u32 v6, v4, v3
	v_add_u32_e32 v4, v6, v4
	v_cmp_ne_u32_e32 vcc, v5, v4
	s_and_saveexec_b64 s[8:9], vcc
	s_xor_b64 s[8:9], exec, s[8:9]
	s_cbranch_execz .LBB0_1160
	s_waitcnt lgkmcnt(0)
	v_mad_u32_u24 v5, v3, v2, v2
	v_mov_b32_e32 v2, 0x4000
	global_load_dword v2, v2, s[70:71] offset:1024 sc1
	s_add_u32 s14, s70, 0x4400
	s_addc_u32 s15, s71, 0
	s_waitcnt vmcnt(0)
	v_cmp_lt_u32_e32 vcc, v2, v5
	s_and_saveexec_b64 s[10:11], vcc
	s_cbranch_execz .LBB0_1159
	s_add_u32 s12, s70, 0x1200
	s_addc_u32 s13, s71, 0
	s_mov_b32 s18, 1
	s_mov_b64 s[16:17], 0
	v_mov_b32_e32 v2, 0
	s_branch .LBB0_1150

; __device__ __forceinline__ unsigned xb_ld(unsigned* p)              { return __hip_atomic_load(p, __ATOMIC_RELAXED, __HIP_MEMORY_SCOPE_AGENT); }
; #define XB_SPIN(cond, bar) do { unsigned _sp = 0; while (cond) { __builtin_amdgcn_s_sleep(1); \
;     if ((++_sp & 255u) == 0u) { if (xb_ld(&(bar)[XB_TMO])) break; if (_sp > XB_SPIN_CAP) { atomicAdd(&(bar)[XB_TMO], 1u); break; } } } } while (0)
; __device__ __forceinline__ void xcd_barrier(const XcdBarrier& b) {
;     ...
;             XB_SPIN(xb_ld(&bar[XB_XGEN(b.x)]) == gen, bar);
.LBB0_1152:
	global_load_dword v4, v2, s[14:15] sc1
	s_add_i32 s18, s18, 1
	s_mov_b64 s[38:39], -1
	s_waitcnt vmcnt(0)
	v_cmp_ge_u32_e32 vcc, v4, v5
	s_orn2_b64 s[26:27], vcc, exec
	s_branch .LBB0_1149

; __device__ __forceinline__ unsigned xb_ld(unsigned* p)              { return __hip_atomic_load(p, __ATOMIC_RELAXED, __HIP_MEMORY_SCOPE_AGENT); }
; __device__ __forceinline__ unsigned xb_add(unsigned* p, unsigned v) { return __hip_atomic_fetch_add(p, v, __ATOMIC_RELAXED, __HIP_MEMORY_SCOPE_AGENT); }
; #define XB_SPIN(cond, bar) do { unsigned _sp = 0; while (cond) { __builtin_amdgcn_s_sleep(1); \
;     if ((++_sp & 255u) == 0u) { if (xb_ld(&(bar)[XB_TMO])) break; if (_sp > XB_SPIN_CAP) { atomicAdd(&(bar)[XB_TMO], 1u); break; } } } } while (0)
; __device__ __forceinline__ void xcd_barrier(const XcdBarrier& b) {
;     ...
;         if (old + 1u == (gen + 1u) * nloc) {
;             __builtin_amdgcn_fence(__ATOMIC_RELEASE, "agent");
;             asm volatile("s_waitcnt vmcnt(0)" ::: "memory");
;             const unsigned og = xb_add(&bar[XB_TOP], 1u);
;             const unsigned tg = og / nx;
;             if (og + 1u == (tg + 1u) * nx) xb_add(&bar[XB_TOPGEN], 1u);
;             else XB_SPIN(xb_ld(&bar[XB_TOPGEN]) == tg, bar);
.LBB0_1163:
	s_or_b64 exec, exec, s[12:13]
	v_cvt_f32_u32_e32 v5, v2
	s_waitcnt vmcnt(0)
	v_readfirstlane_b32 s10, v4
	s_add_u32 s12, s70, 0x4500
	s_addc_u32 s13, s71, 0
	v_rcp_iflag_f32_e32 v5, v5
	v_add_u32_e32 v3, s10, v3
	v_add_u32_e32 v6, 1, v3
	s_mov_b64 s[14:15], -1
	v_mul_f32_e32 v4, 0x4f7ffffe, v5
	v_cvt_u32_f32_e32 v4, v4
	v_sub_u32_e32 v5, 0, v2
	v_mul_lo_u32 v5, v5, v4
	v_mul_hi_u32 v5, v4, v5
	v_add_u32_e32 v4, v4, v5
	v_mul_hi_u32 v4, v3, v4
	v_mul_lo_u32 v5, v4, v2
	v_sub_u32_e32 v3, v3, v5
	v_add_u32_e32 v7, 1, v4
	v_cmp_ge_u32_e32 vcc, v3, v2
	v_sub_u32_e32 v5, v3, v2
	s_nop 0
	v_cndmask_b32_e32 v4, v4, v7, vcc
	v_cndmask_b32_e32 v3, v3, v5, vcc
	v_add_u32_e32 v5, 1, v4
	v_cmp_ge_u32_e32 vcc, v3, v2
	s_nop 1
	v_cndmask_b32_e32 v4, v4, v5, vcc
	v_mul_lo_u32 v3, v2, v4
	v_add_u32_e32 v2, v3, v2
	v_cmp_ne_u32_e32 vcc, v6, v2
	v_mov_b32_e32 v6, v2
	v_mov_b64_e32 v[2:3], s[12:13]
	s_and_saveexec_b64 s[10:11], vcc
	s_cbranch_execz .LBB0_1175
	v_mov_b32_e32 v2, 0
	global_load_dword v3, v2, s[12:13] offset:-256 sc1
	s_mov_b64 s[22:23], 0
	s_waitcnt vmcnt(0)
	v_cmp_lt_u32_e32 vcc, v3, v6
	s_and_saveexec_b64 s[16:17], vcc
	s_cbranch_execz .LBB0_1174
	s_add_u32 s14, s70, 0x1200
	s_addc_u32 s15, s71, 0
	s_mov_b32 s18, 1
	s_branch .LBB0_1167

; __device__ __forceinline__ unsigned xb_ld(unsigned* p)              { return __hip_atomic_load(p, __ATOMIC_RELAXED, __HIP_MEMORY_SCOPE_AGENT); }
; #define XB_SPIN(cond, bar) do { unsigned _sp = 0; while (cond) { __builtin_amdgcn_s_sleep(1); \
;     if ((++_sp & 255u) == 0u) { if (xb_ld(&(bar)[XB_TMO])) break; if (_sp > XB_SPIN_CAP) { atomicAdd(&(bar)[XB_TMO], 1u); break; } } } } while (0)
; __device__ __forceinline__ void xcd_barrier(const XcdBarrier& b) {
;     ...
;             else XB_SPIN(xb_ld(&bar[XB_TOPGEN]) == tg, bar);
.LBB0_1169:
	global_load_dword v3, v2, s[12:13] offset:-256 sc1
	s_add_i32 s18, s18, 1
	s_mov_b64 s[38:39], -1
	s_waitcnt vmcnt(0)
	v_cmp_ge_u32_e32 vcc, v3, v6
	s_orn2_b64 s[42:43], vcc, exec
	s_branch .LBB0_1166

; __device__ __forceinline__ unsigned xb_ld(unsigned* p)              { return __hip_atomic_load(p, __ATOMIC_RELAXED, __HIP_MEMORY_SCOPE_AGENT); }
; __device__ __forceinline__ unsigned xb_add(unsigned* p, unsigned v) { return __hip_atomic_fetch_add(p, v, __ATOMIC_RELAXED, __HIP_MEMORY_SCOPE_AGENT); }
; #define XB_SPIN(cond, bar) do { unsigned _sp = 0; while (cond) { __builtin_amdgcn_s_sleep(1); \
;     if ((++_sp & 255u) == 0u) { if (xb_ld(&(bar)[XB_TMO])) break; if (_sp > XB_SPIN_CAP) { atomicAdd(&(bar)[XB_TMO], 1u); break; } } } } while (0)
; __device__ __forceinline__ void xcd_barrier(const XcdBarrier& b) {
;     ...
;         const unsigned old = xb_add(&bar[XB_XSUB(b.x)], 1u);
;         const unsigned gen = old / nloc;
;         if (old + 1u == (gen + 1u) * nloc) {
;             __builtin_amdgcn_fence(__ATOMIC_RELEASE, "agent");
;             asm volatile("s_waitcnt vmcnt(0)" ::: "memory");
;             const unsigned og = xb_add(&bar[XB_TOP], 1u);
;             const unsigned tg = og / nx;
;             if (og + 1u == (tg + 1u) * nx) xb_add(&bar[XB_TOPGEN], 1u);
;             else XB_SPIN(xb_ld(&bar[XB_TOPGEN]) == tg, bar);
;             xb_add(&bar[XB_XGEN(b.x)], 1u);
;             __builtin_amdgcn_fence(__ATOMIC_ACQUIRE, "agent");
;         } else {
;             XB_SPIN(xb_ld(&bar[XB_XGEN(b.x)]) == gen, bar);
.LBB0_1208:
	s_or_b64 exec, exec, s[12:13]
	v_cvt_f32_u32_e32 v5, v3
	s_waitcnt vmcnt(0)
	v_readfirstlane_b32 s10, v4
	v_sub_u32_e32 v4, 0, v3
	v_rcp_iflag_f32_e32 v5, v5
	v_add_u32_e32 v6, s10, v2
	v_mul_f32_e32 v5, 0x4f7ffffe, v5
	v_cvt_u32_f32_e32 v5, v5
	v_mul_lo_u32 v2, v4, v5
	v_mul_hi_u32 v2, v5, v2
	v_add_u32_e32 v2, v5, v2
	v_mul_hi_u32 v2, v6, v2
	v_mul_lo_u32 v4, v2, v3
	v_sub_u32_e32 v4, v6, v4
	v_add_u32_e32 v5, 1, v2
	v_cmp_ge_u32_e32 vcc, v4, v3
	s_nop 1
	v_cndmask_b32_e32 v2, v2, v5, vcc
	v_sub_u32_e32 v5, v4, v3
	v_cndmask_b32_e32 v4, v4, v5, vcc
	v_add_u32_e32 v5, 1, v2
	v_cmp_ge_u32_e32 vcc, v4, v3
	v_add_u32_e32 v4, 1, v6
	s_nop 0
	v_cndmask_b32_e32 v2, v2, v5, vcc
	v_mul_lo_u32 v5, v3, v2
	v_add_u32_e32 v3, v5, v3
	v_cmp_ne_u32_e32 vcc, v4, v3
	s_and_saveexec_b64 s[10:11], vcc
	s_xor_b64 s[10:11], exec, s[10:11]
	s_cbranch_execz .LBB0_1222
	s_waitcnt lgkmcnt(0)
	v_mad_u32_u24 v4, v2, v1, v1
	v_mov_b32_e32 v1, 0x4000
	global_load_dword v1, v1, s[70:71] offset:1024 sc1
	s_add_u32 s16, s70, 0x4400
	s_addc_u32 s17, s71, 0
	s_waitcnt vmcnt(0)
	v_cmp_lt_u32_e32 vcc, v1, v4
	s_and_saveexec_b64 s[12:13], vcc
	s_cbranch_execz .LBB0_1221
	s_add_u32 s14, s70, 0x1200
	s_addc_u32 s15, s71, 0
	s_mov_b32 s24, 1
	s_mov_b64 s[18:19], 0
	v_mov_b32_e32 v1, 0
	s_branch .LBB0_1212

; __device__ __forceinline__ unsigned xb_ld(unsigned* p)              { return __hip_atomic_load(p, __ATOMIC_RELAXED, __HIP_MEMORY_SCOPE_AGENT); }
; #define XB_SPIN(cond, bar) do { unsigned _sp = 0; while (cond) { __builtin_amdgcn_s_sleep(1); \
;     if ((++_sp & 255u) == 0u) { if (xb_ld(&(bar)[XB_TMO])) break; if (_sp > XB_SPIN_CAP) { atomicAdd(&(bar)[XB_TMO], 1u); break; } } } } while (0)
; __device__ __forceinline__ void xcd_barrier(const XcdBarrier& b) {
;     ...
;             XB_SPIN(xb_ld(&bar[XB_XGEN(b.x)]) == gen, bar);
.LBB0_1214:
	global_load_dword v3, v1, s[16:17] sc1
	s_add_i32 s24, s24, 1
	s_mov_b64 s[26:27], -1
	s_waitcnt vmcnt(0)
	v_cmp_ge_u32_e32 vcc, v3, v4
	s_orn2_b64 s[22:23], vcc, exec
	s_branch .LBB0_1211

; __device__ __forceinline__ unsigned xb_ld(unsigned* p)              { return __hip_atomic_load(p, __ATOMIC_RELAXED, __HIP_MEMORY_SCOPE_AGENT); }
; __device__ __forceinline__ unsigned xb_add(unsigned* p, unsigned v) { return __hip_atomic_fetch_add(p, v, __ATOMIC_RELAXED, __HIP_MEMORY_SCOPE_AGENT); }
; #define XB_SPIN(cond, bar) do { unsigned _sp = 0; while (cond) { __builtin_amdgcn_s_sleep(1); \
;     if ((++_sp & 255u) == 0u) { if (xb_ld(&(bar)[XB_TMO])) break; if (_sp > XB_SPIN_CAP) { atomicAdd(&(bar)[XB_TMO], 1u); break; } } } } while (0)
; __device__ __forceinline__ void xcd_barrier(const XcdBarrier& b) {
;     ...
;         if (old + 1u == (gen + 1u) * nloc) {
;             __builtin_amdgcn_fence(__ATOMIC_RELEASE, "agent");
;             asm volatile("s_waitcnt vmcnt(0)" ::: "memory");
;             const unsigned og = xb_add(&bar[XB_TOP], 1u);
;             const unsigned tg = og / nx;
;             if (og + 1u == (tg + 1u) * nx) xb_add(&bar[XB_TOPGEN], 1u);
;             else XB_SPIN(xb_ld(&bar[XB_TOPGEN]) == tg, bar);
.LBB0_1225:
	s_or_b64 exec, exec, s[14:15]
	v_cvt_f32_u32_e32 v4, v1
	s_waitcnt vmcnt(0)
	v_readfirstlane_b32 s12, v3
	s_add_u32 s14, s70, 0x4500
	s_addc_u32 s15, s71, 0
	v_rcp_iflag_f32_e32 v4, v4
	v_add_u32_e32 v2, s12, v2
	v_add_u32_e32 v5, 1, v2
	s_mov_b64 s[16:17], -1
	v_mul_f32_e32 v3, 0x4f7ffffe, v4
	v_cvt_u32_f32_e32 v3, v3
	v_sub_u32_e32 v4, 0, v1
	v_mul_lo_u32 v4, v4, v3
	v_mul_hi_u32 v4, v3, v4
	v_add_u32_e32 v3, v3, v4
	v_mul_hi_u32 v3, v2, v3
	v_mul_lo_u32 v4, v3, v1
	v_sub_u32_e32 v2, v2, v4
	v_add_u32_e32 v6, 1, v3
	v_cmp_ge_u32_e32 vcc, v2, v1
	v_sub_u32_e32 v4, v2, v1
	s_nop 0
	v_cndmask_b32_e32 v3, v3, v6, vcc
	v_cndmask_b32_e32 v2, v2, v4, vcc
	v_add_u32_e32 v4, 1, v3
	v_cmp_ge_u32_e32 vcc, v2, v1
	s_nop 1
	v_cndmask_b32_e32 v4, v3, v4, vcc
	v_mul_lo_u32 v2, v1, v4
	v_add_u32_e32 v1, v2, v1
	v_cmp_ne_u32_e32 vcc, v5, v1
	v_mov_b32_e32 v5, v1
	v_mov_b64_e32 v[2:3], s[14:15]
	s_and_saveexec_b64 s[12:13], vcc
	s_cbranch_execz .LBB0_1237
	v_mov_b32_e32 v1, 0
	global_load_dword v2, v1, s[14:15] offset:-256 sc1
	s_mov_b64 s[20:21], 0
	s_waitcnt vmcnt(0)
	v_cmp_lt_u32_e32 vcc, v2, v5
	s_and_saveexec_b64 s[18:19], vcc
	s_cbranch_execz .LBB0_1236
	s_add_u32 s16, s70, 0x1200
	s_addc_u32 s17, s71, 0
	s_mov_b32 s24, 1
	s_branch .LBB0_1229

; __device__ __forceinline__ unsigned xb_ld(unsigned* p)              { return __hip_atomic_load(p, __ATOMIC_RELAXED, __HIP_MEMORY_SCOPE_AGENT); }
; #define XB_SPIN(cond, bar) do { unsigned _sp = 0; while (cond) { __builtin_amdgcn_s_sleep(1); \
;     if ((++_sp & 255u) == 0u) { if (xb_ld(&(bar)[XB_TMO])) break; if (_sp > XB_SPIN_CAP) { atomicAdd(&(bar)[XB_TMO], 1u); break; } } } } while (0)
; __device__ __forceinline__ void xcd_barrier(const XcdBarrier& b) {
;     ...
;             else XB_SPIN(xb_ld(&bar[XB_TOPGEN]) == tg, bar);
.LBB0_1231:
	global_load_dword v2, v1, s[14:15] offset:-256 sc1
	s_add_i32 s24, s24, 1
	s_mov_b64 s[26:27], -1
	s_waitcnt vmcnt(0)
	v_cmp_ge_u32_e32 vcc, v2, v5
	s_orn2_b64 s[40:41], vcc, exec
	s_branch .LBB0_1228

; __device__ __forceinline__ unsigned xb_ld(unsigned* p)              { return __hip_atomic_load(p, __ATOMIC_RELAXED, __HIP_MEMORY_SCOPE_AGENT); }
; __device__ __forceinline__ unsigned xb_add(unsigned* p, unsigned v) { return __hip_atomic_fetch_add(p, v, __ATOMIC_RELAXED, __HIP_MEMORY_SCOPE_AGENT); }
; #define XB_SPIN(cond, bar) do { unsigned _sp = 0; while (cond) { __builtin_amdgcn_s_sleep(1); \
;     if ((++_sp & 255u) == 0u) { if (xb_ld(&(bar)[XB_TMO])) break; if (_sp > XB_SPIN_CAP) { atomicAdd(&(bar)[XB_TMO], 1u); break; } } } } while (0)
; __device__ __forceinline__ void xcd_barrier(const XcdBarrier& b) {
;     ...
;         const unsigned old = xb_add(&bar[XB_XSUB(b.x)], 1u);
;         const unsigned gen = old / nloc;
;         if (old + 1u == (gen + 1u) * nloc) {
;             __builtin_amdgcn_fence(__ATOMIC_RELEASE, "agent");
;             asm volatile("s_waitcnt vmcnt(0)" ::: "memory");
;             const unsigned og = xb_add(&bar[XB_TOP], 1u);
;             const unsigned tg = og / nx;
;             if (og + 1u == (tg + 1u) * nx) xb_add(&bar[XB_TOPGEN], 1u);
;             else XB_SPIN(xb_ld(&bar[XB_TOPGEN]) == tg, bar);
;             xb_add(&bar[XB_XGEN(b.x)], 1u);
;             __builtin_amdgcn_fence(__ATOMIC_ACQUIRE, "agent");
;         } else {
;             XB_SPIN(xb_ld(&bar[XB_XGEN(b.x)]) == gen, bar);
.LBB0_1363:
	s_or_b64 exec, exec, s[14:15]
	v_cvt_f32_u32_e32 v5, v3
	s_waitcnt vmcnt(0)
	v_readfirstlane_b32 s12, v4
	v_sub_u32_e32 v4, 0, v3
	v_rcp_iflag_f32_e32 v5, v5
	v_add_u32_e32 v6, s12, v2
	v_mul_f32_e32 v5, 0x4f7ffffe, v5
	v_cvt_u32_f32_e32 v5, v5
	v_mul_lo_u32 v2, v4, v5
	v_mul_hi_u32 v2, v5, v2
	v_add_u32_e32 v2, v5, v2
	v_mul_hi_u32 v2, v6, v2
	v_mul_lo_u32 v4, v2, v3
	v_sub_u32_e32 v4, v6, v4
	v_add_u32_e32 v5, 1, v2
	v_cmp_ge_u32_e32 vcc, v4, v3
	s_nop 1
	v_cndmask_b32_e32 v2, v2, v5, vcc
	v_sub_u32_e32 v5, v4, v3
	v_cndmask_b32_e32 v4, v4, v5, vcc
	v_add_u32_e32 v5, 1, v2
	v_cmp_ge_u32_e32 vcc, v4, v3
	v_add_u32_e32 v4, 1, v6
	s_nop 0
	v_cndmask_b32_e32 v2, v2, v5, vcc
	v_mul_lo_u32 v5, v3, v2
	v_add_u32_e32 v3, v5, v3
	v_cmp_ne_u32_e32 vcc, v4, v3
	s_and_saveexec_b64 s[12:13], vcc
	s_xor_b64 s[12:13], exec, s[12:13]
	s_cbranch_execz .LBB0_1377
	s_waitcnt lgkmcnt(0)
	v_mad_u32_u24 v4, v2, v1, v1
	v_mov_b32_e32 v1, 0x4000
	global_load_dword v1, v1, s[70:71] offset:1024 sc1
	s_add_u32 s18, s70, 0x4400
	s_addc_u32 s19, s71, 0
	s_waitcnt vmcnt(0)
	v_cmp_lt_u32_e32 vcc, v1, v4
	s_and_saveexec_b64 s[14:15], vcc
	s_cbranch_execz .LBB0_1376
	s_add_u32 s16, s70, 0x1200
	s_addc_u32 s17, s71, 0
	s_mov_b32 s24, 1
	s_mov_b64 s[20:21], 0
	v_mov_b32_e32 v1, 0
	s_branch .LBB0_1367

; __device__ __forceinline__ unsigned xb_ld(unsigned* p)              { return __hip_atomic_load(p, __ATOMIC_RELAXED, __HIP_MEMORY_SCOPE_AGENT); }
; #define XB_SPIN(cond, bar) do { unsigned _sp = 0; while (cond) { __builtin_amdgcn_s_sleep(1); \
;     if ((++_sp & 255u) == 0u) { if (xb_ld(&(bar)[XB_TMO])) break; if (_sp > XB_SPIN_CAP) { atomicAdd(&(bar)[XB_TMO], 1u); break; } } } } while (0)
; __device__ __forceinline__ void xcd_barrier(const XcdBarrier& b) {
;     ...
;             XB_SPIN(xb_ld(&bar[XB_XGEN(b.x)]) == gen, bar);
.LBB0_1369:
	global_load_dword v3, v1, s[18:19] sc1
	s_add_i32 s24, s24, 1
	s_mov_b64 s[38:39], -1
	s_waitcnt vmcnt(0)
	v_cmp_ge_u32_e32 vcc, v3, v4
	s_orn2_b64 s[26:27], vcc, exec
	s_branch .LBB0_1366

; __device__ __forceinline__ unsigned xb_ld(unsigned* p)              { return __hip_atomic_load(p, __ATOMIC_RELAXED, __HIP_MEMORY_SCOPE_AGENT); }
; __device__ __forceinline__ unsigned xb_add(unsigned* p, unsigned v) { return __hip_atomic_fetch_add(p, v, __ATOMIC_RELAXED, __HIP_MEMORY_SCOPE_AGENT); }
; #define XB_SPIN(cond, bar) do { unsigned _sp = 0; while (cond) { __builtin_amdgcn_s_sleep(1); \
;     if ((++_sp & 255u) == 0u) { if (xb_ld(&(bar)[XB_TMO])) break; if (_sp > XB_SPIN_CAP) { atomicAdd(&(bar)[XB_TMO], 1u); break; } } } } while (0)
; __device__ __forceinline__ void xcd_barrier(const XcdBarrier& b) {
;     ...
;         const unsigned old = xb_add(&bar[XB_XSUB(b.x)], 1u);
;         const unsigned gen = old / nloc;
;         if (old + 1u == (gen + 1u) * nloc) {
;             __builtin_amdgcn_fence(__ATOMIC_RELEASE, "agent");
;             asm volatile("s_waitcnt vmcnt(0)" ::: "memory");
;             const unsigned og = xb_add(&bar[XB_TOP], 1u);
;             const unsigned tg = og / nx;
;             if (og + 1u == (tg + 1u) * nx) xb_add(&bar[XB_TOPGEN], 1u);
;             else XB_SPIN(xb_ld(&bar[XB_TOPGEN]) == tg, bar);
.LBB0_1380:
	s_or_b64 exec, exec, s[16:17]
	v_cvt_f32_u32_e32 v4, v1
	s_waitcnt vmcnt(0)
	v_readfirstlane_b32 s14, v3
	s_add_u32 s16, s70, 0x4500
	s_addc_u32 s17, s71, 0
	v_rcp_iflag_f32_e32 v4, v4
	v_add_u32_e32 v2, s14, v2
	v_add_u32_e32 v5, 1, v2
	s_mov_b64 s[18:19], -1
	v_mul_f32_e32 v3, 0x4f7ffffe, v4
	v_cvt_u32_f32_e32 v3, v3
	v_sub_u32_e32 v4, 0, v1
	v_mul_lo_u32 v4, v4, v3
	v_mul_hi_u32 v4, v3, v4
	v_add_u32_e32 v3, v3, v4
	v_mul_hi_u32 v3, v2, v3
	v_mul_lo_u32 v4, v3, v1
	v_sub_u32_e32 v2, v2, v4
	v_add_u32_e32 v6, 1, v3
	v_cmp_ge_u32_e32 vcc, v2, v1
	v_sub_u32_e32 v4, v2, v1
	s_nop 0
	v_cndmask_b32_e32 v3, v3, v6, vcc
	v_cndmask_b32_e32 v2, v2, v4, vcc
	v_add_u32_e32 v4, 1, v3
	v_cmp_ge_u32_e32 vcc, v2, v1
	s_nop 1
	v_cndmask_b32_e32 v4, v3, v4, vcc
	v_mul_lo_u32 v2, v1, v4
	v_add_u32_e32 v1, v2, v1
	v_cmp_ne_u32_e32 vcc, v5, v1
	v_mov_b32_e32 v5, v1
	v_mov_b64_e32 v[2:3], s[16:17]
	s_and_saveexec_b64 s[14:15], vcc
	s_cbranch_execz .LBB0_1392
	v_mov_b32_e32 v1, 0
	global_load_dword v2, v1, s[16:17] offset:-256 sc1
	s_mov_b64 s[22:23], 0
	s_waitcnt vmcnt(0)
	v_cmp_lt_u32_e32 vcc, v2, v5
	s_and_saveexec_b64 s[20:21], vcc
	s_cbranch_execz .LBB0_1391
	s_add_u32 s18, s70, 0x1200
	s_addc_u32 s19, s71, 0
	s_mov_b32 s24, 1
	s_branch .LBB0_1384

; __device__ __forceinline__ unsigned xb_ld(unsigned* p)              { return __hip_atomic_load(p, __ATOMIC_RELAXED, __HIP_MEMORY_SCOPE_AGENT); }
; #define XB_SPIN(cond, bar) do { unsigned _sp = 0; while (cond) { __builtin_amdgcn_s_sleep(1); \
;     if ((++_sp & 255u) == 0u) { if (xb_ld(&(bar)[XB_TMO])) break; if (_sp > XB_SPIN_CAP) { atomicAdd(&(bar)[XB_TMO], 1u); break; } } } } while (0)
; __device__ __forceinline__ void xcd_barrier(const XcdBarrier& b) {
;     ...
;             else XB_SPIN(xb_ld(&bar[XB_TOPGEN]) == tg, bar);
.LBB0_1386:
	global_load_dword v2, v1, s[16:17] offset:-256 sc1
	s_add_i32 s24, s24, 1
	s_mov_b64 s[38:39], -1
	s_waitcnt vmcnt(0)
	v_cmp_ge_u32_e32 vcc, v2, v5
	s_orn2_b64 s[42:43], vcc, exec
	s_branch .LBB0_1383

; __device__ __forceinline__ unsigned xb_ld(unsigned* p)              { return __hip_atomic_load(p, __ATOMIC_RELAXED, __HIP_MEMORY_SCOPE_AGENT); }
; __device__ __forceinline__ unsigned xb_add(unsigned* p, unsigned v) { return __hip_atomic_fetch_add(p, v, __ATOMIC_RELAXED, __HIP_MEMORY_SCOPE_AGENT); }
; #define XB_SPIN(cond, bar) do { unsigned _sp = 0; while (cond) { __builtin_amdgcn_s_sleep(1); \
;     if ((++_sp & 255u) == 0u) { if (xb_ld(&(bar)[XB_TMO])) break; if (_sp > XB_SPIN_CAP) { atomicAdd(&(bar)[XB_TMO], 1u); break; } } } } while (0)
; __device__ __forceinline__ void xcd_barrier(const XcdBarrier& b) {
;     ...
;         const unsigned old = xb_add(&bar[XB_XSUB(b.x)], 1u);
;         const unsigned gen = old / nloc;
;         if (old + 1u == (gen + 1u) * nloc) {
;     ...
;         } else {
;             XB_SPIN(xb_ld(&bar[XB_XGEN(b.x)]) == gen, bar);
;             __builtin_amdgcn_fence(__ATOMIC_ACQUIRE, "agent");
.LBB0_1434:
	s_or_b64 exec, exec, s[18:19]
	v_cvt_f32_u32_e32 v5, v3
	s_waitcnt vmcnt(0)
	v_readfirstlane_b32 s16, v4
	v_sub_u32_e32 v4, 0, v3
	v_rcp_iflag_f32_e32 v5, v5
	v_add_u32_e32 v6, s16, v2
	v_mul_f32_e32 v5, 0x4f7ffffe, v5
	v_cvt_u32_f32_e32 v5, v5
	v_mul_lo_u32 v2, v4, v5
	v_mul_hi_u32 v2, v5, v2
	v_add_u32_e32 v2, v5, v2
	v_mul_hi_u32 v2, v6, v2
	v_mul_lo_u32 v4, v2, v3
	v_sub_u32_e32 v4, v6, v4
	v_add_u32_e32 v5, 1, v2
	v_cmp_ge_u32_e32 vcc, v4, v3
	s_nop 1
	v_cndmask_b32_e32 v2, v2, v5, vcc
	v_sub_u32_e32 v5, v4, v3
	v_cndmask_b32_e32 v4, v4, v5, vcc
	v_add_u32_e32 v5, 1, v2
	v_cmp_ge_u32_e32 vcc, v4, v3
	v_add_u32_e32 v4, 1, v6
	s_nop 0
	v_cndmask_b32_e32 v2, v2, v5, vcc
	v_mul_lo_u32 v5, v3, v2
	v_add_u32_e32 v3, v5, v3
	v_cmp_ne_u32_e32 vcc, v4, v3
	s_and_saveexec_b64 s[16:17], vcc
	s_xor_b64 s[16:17], exec, s[16:17]
	s_cbranch_execz .LBB0_1448
	s_waitcnt lgkmcnt(0)
	v_mad_u32_u24 v4, v2, v1, v1
	v_mov_b32_e32 v1, 0x4000
	global_load_dword v1, v1, s[70:71] offset:1024 sc1
	s_add_u32 s22, s70, 0x4400
	s_addc_u32 s23, s71, 0
	s_waitcnt vmcnt(0)
	v_cmp_lt_u32_e32 vcc, v1, v4
	s_and_saveexec_b64 s[18:19], vcc
	s_cbranch_execz .LBB0_1447
	s_add_u32 s20, s70, 0x1200
	s_addc_u32 s21, s71, 0
	s_mov_b32 s24, 1
	s_mov_b64 s[26:27], 0
	v_mov_b32_e32 v1, 0
	s_branch .LBB0_1438

; __device__ __forceinline__ unsigned xb_ld(unsigned* p)              { return __hip_atomic_load(p, __ATOMIC_RELAXED, __HIP_MEMORY_SCOPE_AGENT); }
; #define XB_SPIN(cond, bar) do { unsigned _sp = 0; while (cond) { __builtin_amdgcn_s_sleep(1); \
;     if ((++_sp & 255u) == 0u) { if (xb_ld(&(bar)[XB_TMO])) break; if (_sp > XB_SPIN_CAP) { atomicAdd(&(bar)[XB_TMO], 1u); break; } } } } while (0)
; __device__ __forceinline__ void xcd_barrier(const XcdBarrier& b) {
;     ...
;             XB_SPIN(xb_ld(&bar[XB_XGEN(b.x)]) == gen, bar);
.LBB0_1440:
	global_load_dword v3, v1, s[22:23] sc1
	s_add_i32 s24, s24, 1
	s_mov_b64 s[40:41], -1
	s_waitcnt vmcnt(0)
	v_cmp_ge_u32_e32 vcc, v3, v4
	s_orn2_b64 s[38:39], vcc, exec
	s_branch .LBB0_1437

; __device__ __forceinline__ unsigned xb_ld(unsigned* p)              { return __hip_atomic_load(p, __ATOMIC_RELAXED, __HIP_MEMORY_SCOPE_AGENT); }
; __device__ __forceinline__ unsigned xb_add(unsigned* p, unsigned v) { return __hip_atomic_fetch_add(p, v, __ATOMIC_RELAXED, __HIP_MEMORY_SCOPE_AGENT); }
; #define XB_SPIN(cond, bar) do { unsigned _sp = 0; while (cond) { __builtin_amdgcn_s_sleep(1); \
;     if ((++_sp & 255u) == 0u) { if (xb_ld(&(bar)[XB_TMO])) break; if (_sp > XB_SPIN_CAP) { atomicAdd(&(bar)[XB_TMO], 1u); break; } } } } while (0)
; __device__ __forceinline__ void xcd_barrier(const XcdBarrier& b) {
;     ...
;         const unsigned old = xb_add(&bar[XB_XSUB(b.x)], 1u);
;         const unsigned gen = old / nloc;
;         if (old + 1u == (gen + 1u) * nloc) {
;             __builtin_amdgcn_fence(__ATOMIC_RELEASE, "agent");
;             asm volatile("s_waitcnt vmcnt(0)" ::: "memory");
;             const unsigned og = xb_add(&bar[XB_TOP], 1u);
;             const unsigned tg = og / nx;
;             if (og + 1u == (tg + 1u) * nx) xb_add(&bar[XB_TOPGEN], 1u);
;             else XB_SPIN(xb_ld(&bar[XB_TOPGEN]) == tg, bar);
.LBB0_1451:
	s_or_b64 exec, exec, s[20:21]
	v_cvt_f32_u32_e32 v4, v1
	s_waitcnt vmcnt(0)
	v_readfirstlane_b32 s18, v3
	s_add_u32 s20, s70, 0x4500
	s_addc_u32 s21, s71, 0
	v_rcp_iflag_f32_e32 v4, v4
	v_add_u32_e32 v2, s18, v2
	v_add_u32_e32 v5, 1, v2
	s_mov_b64 s[22:23], -1
	v_mul_f32_e32 v3, 0x4f7ffffe, v4
	v_cvt_u32_f32_e32 v3, v3
	v_sub_u32_e32 v4, 0, v1
	v_mul_lo_u32 v4, v4, v3
	v_mul_hi_u32 v4, v3, v4
	v_add_u32_e32 v3, v3, v4
	v_mul_hi_u32 v3, v2, v3
	v_mul_lo_u32 v4, v3, v1
	v_sub_u32_e32 v2, v2, v4
	v_add_u32_e32 v6, 1, v3
	v_cmp_ge_u32_e32 vcc, v2, v1
	v_sub_u32_e32 v4, v2, v1
	s_nop 0
	v_cndmask_b32_e32 v3, v3, v6, vcc
	v_cndmask_b32_e32 v2, v2, v4, vcc
	v_add_u32_e32 v4, 1, v3
	v_cmp_ge_u32_e32 vcc, v2, v1
	s_nop 1
	v_cndmask_b32_e32 v4, v3, v4, vcc
	v_mul_lo_u32 v2, v1, v4
	v_add_u32_e32 v1, v2, v1
	v_cmp_ne_u32_e32 vcc, v5, v1
	v_mov_b32_e32 v5, v1
	v_mov_b64_e32 v[2:3], s[20:21]
	s_and_saveexec_b64 s[18:19], vcc
	s_cbranch_execz .LBB0_1463
	v_mov_b32_e32 v1, 0
	global_load_dword v2, v1, s[20:21] offset:-256 sc1
	s_mov_b64 s[36:37], 0
	s_waitcnt vmcnt(0)
	v_cmp_lt_u32_e32 vcc, v2, v5
	s_and_saveexec_b64 s[26:27], vcc
	s_cbranch_execz .LBB0_1462
	s_add_u32 s22, s70, 0x1200
	s_addc_u32 s23, s71, 0
	s_mov_b32 s24, 1
	s_branch .LBB0_1455

; __device__ __forceinline__ unsigned xb_ld(unsigned* p)              { return __hip_atomic_load(p, __ATOMIC_RELAXED, __HIP_MEMORY_SCOPE_AGENT); }
; #define XB_SPIN(cond, bar) do { unsigned _sp = 0; while (cond) { __builtin_amdgcn_s_sleep(1); \
;     if ((++_sp & 255u) == 0u) { if (xb_ld(&(bar)[XB_TMO])) break; if (_sp > XB_SPIN_CAP) { atomicAdd(&(bar)[XB_TMO], 1u); break; } } } } while (0)
; __device__ __forceinline__ void xcd_barrier(const XcdBarrier& b) {
;     ...
;             else XB_SPIN(xb_ld(&bar[XB_TOPGEN]) == tg, bar);
.LBB0_1457:
	global_load_dword v2, v1, s[20:21] offset:-256 sc1
	s_add_i32 s24, s24, 1
	s_mov_b64 s[40:41], -1
	s_waitcnt vmcnt(0)
	v_cmp_ge_u32_e32 vcc, v2, v5
	s_orn2_b64 s[44:45], vcc, exec
	s_branch .LBB0_1454

; __device__ __forceinline__ unsigned xb_ld(unsigned* p)              { return __hip_atomic_load(p, __ATOMIC_RELAXED, __HIP_MEMORY_SCOPE_AGENT); }
; __device__ __forceinline__ unsigned xb_add(unsigned* p, unsigned v) { return __hip_atomic_fetch_add(p, v, __ATOMIC_RELAXED, __HIP_MEMORY_SCOPE_AGENT); }
; #define XB_SPIN(cond, bar) do { unsigned _sp = 0; while (cond) { __builtin_amdgcn_s_sleep(1); \
;     if ((++_sp & 255u) == 0u) { if (xb_ld(&(bar)[XB_TMO])) break; if (_sp > XB_SPIN_CAP) { atomicAdd(&(bar)[XB_TMO], 1u); break; } } } } while (0)
; __device__ __forceinline__ void xcd_barrier(const XcdBarrier& b) {
;     ...
;         const unsigned old = xb_add(&bar[XB_XSUB(b.x)], 1u);
;         const unsigned gen = old / nloc;
;         if (old + 1u == (gen + 1u) * nloc) {
;     ...
;         } else {
;             XB_SPIN(xb_ld(&bar[XB_XGEN(b.x)]) == gen, bar);
;             __builtin_amdgcn_fence(__ATOMIC_ACQUIRE, "agent");
.LBB0_1522:
	s_or_b64 exec, exec, s[8:9]
	v_cvt_f32_u32_e32 v5, v3
	s_waitcnt vmcnt(0)
	v_readfirstlane_b32 s4, v4
	v_sub_u32_e32 v4, 0, v3
	v_rcp_iflag_f32_e32 v5, v5
	v_add_u32_e32 v6, s4, v2
	v_mul_f32_e32 v5, 0x4f7ffffe, v5
	v_cvt_u32_f32_e32 v5, v5
	v_mul_lo_u32 v2, v4, v5
	v_mul_hi_u32 v2, v5, v2
	v_add_u32_e32 v2, v5, v2
	v_mul_hi_u32 v2, v6, v2
	v_mul_lo_u32 v4, v2, v3
	v_sub_u32_e32 v4, v6, v4
	v_add_u32_e32 v5, 1, v2
	v_cmp_ge_u32_e32 vcc, v4, v3
	s_nop 1
	v_cndmask_b32_e32 v2, v2, v5, vcc
	v_sub_u32_e32 v5, v4, v3
	v_cndmask_b32_e32 v4, v4, v5, vcc
	v_add_u32_e32 v5, 1, v2
	v_cmp_ge_u32_e32 vcc, v4, v3
	v_add_u32_e32 v4, 1, v6
	s_nop 0
	v_cndmask_b32_e32 v2, v2, v5, vcc
	v_mul_lo_u32 v5, v3, v2
	v_add_u32_e32 v3, v5, v3
	v_cmp_ne_u32_e32 vcc, v4, v3
	s_and_saveexec_b64 s[4:5], vcc
	s_xor_b64 s[4:5], exec, s[4:5]
	s_cbranch_execz .LBB0_1536
	s_waitcnt lgkmcnt(0)
	v_mad_u32_u24 v4, v2, v1, v1
	v_mov_b32_e32 v1, 0x4000
	global_load_dword v1, v1, s[70:71] offset:1024 sc1
	s_add_u32 s14, s70, 0x4400
	s_addc_u32 s15, s71, 0
	s_waitcnt vmcnt(0)
	v_cmp_lt_u32_e32 vcc, v1, v4
	s_and_saveexec_b64 s[8:9], vcc
	s_cbranch_execz .LBB0_1535
	s_add_u32 s12, s70, 0x1200
	s_addc_u32 s13, s71, 0
	s_mov_b32 s24, 1
	s_mov_b64 s[16:17], 0
	v_mov_b32_e32 v1, 0
	s_branch .LBB0_1526

; __device__ __forceinline__ unsigned xb_ld(unsigned* p)              { return __hip_atomic_load(p, __ATOMIC_RELAXED, __HIP_MEMORY_SCOPE_AGENT); }
; #define XB_SPIN(cond, bar) do { unsigned _sp = 0; while (cond) { __builtin_amdgcn_s_sleep(1); \
;     if ((++_sp & 255u) == 0u) { if (xb_ld(&(bar)[XB_TMO])) break; if (_sp > XB_SPIN_CAP) { atomicAdd(&(bar)[XB_TMO], 1u); break; } } } } while (0)
; __device__ __forceinline__ void xcd_barrier(const XcdBarrier& b) {
;     ...
;             XB_SPIN(xb_ld(&bar[XB_XGEN(b.x)]) == gen, bar);
.LBB0_1528:
	global_load_dword v3, v1, s[14:15] sc1
	s_add_i32 s24, s24, 1
	s_mov_b64 s[22:23], -1
	s_waitcnt vmcnt(0)
	v_cmp_ge_u32_e32 vcc, v3, v4
	s_orn2_b64 s[20:21], vcc, exec
	s_branch .LBB0_1525

; __device__ __forceinline__ unsigned xb_ld(unsigned* p)              { return __hip_atomic_load(p, __ATOMIC_RELAXED, __HIP_MEMORY_SCOPE_AGENT); }
; __device__ __forceinline__ unsigned xb_add(unsigned* p, unsigned v) { return __hip_atomic_fetch_add(p, v, __ATOMIC_RELAXED, __HIP_MEMORY_SCOPE_AGENT); }
; #define XB_SPIN(cond, bar) do { unsigned _sp = 0; while (cond) { __builtin_amdgcn_s_sleep(1); \
;     if ((++_sp & 255u) == 0u) { if (xb_ld(&(bar)[XB_TMO])) break; if (_sp > XB_SPIN_CAP) { atomicAdd(&(bar)[XB_TMO], 1u); break; } } } } while (0)
; __device__ __forceinline__ void xcd_barrier(const XcdBarrier& b) {
;     ...
;         const unsigned old = xb_add(&bar[XB_XSUB(b.x)], 1u);
;         const unsigned gen = old / nloc;
;         if (old + 1u == (gen + 1u) * nloc) {
;             __builtin_amdgcn_fence(__ATOMIC_RELEASE, "agent");
;             asm volatile("s_waitcnt vmcnt(0)" ::: "memory");
;             const unsigned og = xb_add(&bar[XB_TOP], 1u);
;             const unsigned tg = og / nx;
;             if (og + 1u == (tg + 1u) * nx) xb_add(&bar[XB_TOPGEN], 1u);
;             else XB_SPIN(xb_ld(&bar[XB_TOPGEN]) == tg, bar);
.LBB0_1539:
	s_or_b64 exec, exec, s[12:13]
	v_cvt_f32_u32_e32 v4, v1
	s_waitcnt vmcnt(0)
	v_readfirstlane_b32 s8, v3
	s_add_u32 s12, s70, 0x4500
	s_addc_u32 s13, s71, 0
	v_rcp_iflag_f32_e32 v4, v4
	v_add_u32_e32 v2, s8, v2
	v_add_u32_e32 v5, 1, v2
	s_mov_b64 s[14:15], -1
	v_mul_f32_e32 v3, 0x4f7ffffe, v4
	v_cvt_u32_f32_e32 v3, v3
	v_sub_u32_e32 v4, 0, v1
	v_mul_lo_u32 v4, v4, v3
	v_mul_hi_u32 v4, v3, v4
	v_add_u32_e32 v3, v3, v4
	v_mul_hi_u32 v3, v2, v3
	v_mul_lo_u32 v4, v3, v1
	v_sub_u32_e32 v2, v2, v4
	v_add_u32_e32 v6, 1, v3
	v_cmp_ge_u32_e32 vcc, v2, v1
	v_sub_u32_e32 v4, v2, v1
	s_nop 0
	v_cndmask_b32_e32 v3, v3, v6, vcc
	v_cndmask_b32_e32 v2, v2, v4, vcc
	v_add_u32_e32 v4, 1, v3
	v_cmp_ge_u32_e32 vcc, v2, v1
	s_nop 1
	v_cndmask_b32_e32 v4, v3, v4, vcc
	v_mul_lo_u32 v2, v1, v4
	v_add_u32_e32 v1, v2, v1
	v_cmp_ne_u32_e32 vcc, v5, v1
	v_mov_b32_e32 v5, v1
	v_mov_b64_e32 v[2:3], s[12:13]
	s_and_saveexec_b64 s[8:9], vcc
	s_cbranch_execz .LBB0_1551
	v_mov_b32_e32 v1, 0
	global_load_dword v2, v1, s[12:13] offset:-256 sc1
	s_mov_b64 s[18:19], 0
	s_waitcnt vmcnt(0)
	v_cmp_lt_u32_e32 vcc, v2, v5
	s_and_saveexec_b64 s[16:17], vcc
	s_cbranch_execz .LBB0_1550
	s_add_u32 s14, s70, 0x1200
	s_addc_u32 s15, s71, 0
	s_mov_b32 s24, 1
	s_branch .LBB0_1543

; __device__ __forceinline__ unsigned xb_ld(unsigned* p)              { return __hip_atomic_load(p, __ATOMIC_RELAXED, __HIP_MEMORY_SCOPE_AGENT); }
; #define XB_SPIN(cond, bar) do { unsigned _sp = 0; while (cond) { __builtin_amdgcn_s_sleep(1); \
;     if ((++_sp & 255u) == 0u) { if (xb_ld(&(bar)[XB_TMO])) break; if (_sp > XB_SPIN_CAP) { atomicAdd(&(bar)[XB_TMO], 1u); break; } } } } while (0)
; __device__ __forceinline__ void xcd_barrier(const XcdBarrier& b) {
;     ...
;             else XB_SPIN(xb_ld(&bar[XB_TOPGEN]) == tg, bar);
.LBB0_1545:
	global_load_dword v2, v1, s[12:13] offset:-256 sc1
	s_add_i32 s24, s24, 1
	s_mov_b64 s[22:23], -1
	s_waitcnt vmcnt(0)
	v_cmp_ge_u32_e32 vcc, v2, v5
	s_orn2_b64 s[30:31], vcc, exec
	s_branch .LBB0_1542
